# W1 plus s_setprio 0 moved behind the closing barrier of each compute segment (nothing but the barrier between the last MFMA of one wave and the first MFMA of its partner)
# speedup vs baseline: 1.0093x; 1.0021x over previous
.LBB0_310:
	s_ashr_i32 s91, s90, 31
	s_lshl_b64 s[4:5], s[90:91], 20
	s_add_u32 s62, s66, s4
	s_addc_u32 s63, s67, s5
	s_and_b64 s[4:5], s[36:37], exec
	s_cselect_b32 s4, s63, s25
	s_cselect_b32 s5, s62, s24
	s_ashr_i32 s89, s88, 31
	s_lshl_b64 s[20:21], s[88:89], 20
	s_add_u32 s20, s72, s20
	s_addc_u32 s21, s73, s21
	s_and_b64 s[30:31], s[36:37], exec
	s_cselect_b32 s8, s21, s1
	s_cselect_b32 s13, s20, s0
	s_add_u32 s17, s0, 0x10000
	s_addc_u32 s19, s1, 0
	s_add_u32 s0, s24, 0x80080
	s_addc_u32 s1, s25, 0
	s_mov_b32 s28, -2
	v_add_u32_e32 v100, s3, v190
	v_add_u32_e32 v156, s75, v190
	ds_read_b128 v[40:43], v100
	ds_read_b128 v[60:63], v100 offset:1024
	ds_read_b128 v[80:83], v100 offset:2048
	ds_read_b128 v[100:103], v100 offset:3072
	ds_read_b128 v[120:123], v156
	ds_read_b128 v[140:143], v156 offset:1024
	ds_read_b128 v[152:155], v156 offset:2048
	ds_read_b128 v[156:159], v156 offset:3072
	s_add_u32 s24, s0, 0xfff80080
	s_addc_u32 s25, s1, -1
	s_cmp_eq_u32 s28, 28
	s_cselect_b32 s39, s4, s25
	s_cselect_b32 s38, s5, s24
	s_cselect_b32 s25, s8, s19
	s_cselect_b32 s24, s13, s17
	v_lshl_add_u64 v[188:189], s[0:1], 0, v[168:169]
	s_add_i32 m0, s78, 0xc000
	ds_read_b128 v[172:175], v191
	ds_read_b128 v[176:179], v191 offset:1024
	ds_read_b128 v[180:183], v191 offset:2048
	ds_read_b128 v[184:187], v191 offset:3072
	ds_read_b128 v[192:195], v191 offset:4096
	ds_read_b128 v[196:199], v191 offset:5120
	ds_read_b128 v[200:203], v191 offset:6144
	ds_read_b128 v[204:207], v191 offset:7168
	global_load_lds_dwordx4 v[188:189], off
	v_lshl_add_u64 v[188:189], s[0:1], 0, v[170:171]
	s_add_i32 m0, s78, 0xe000
	s_nop 0
	global_load_lds_dwordx4 v[188:189], off
	s_waitcnt vmcnt(8)
	s_waitcnt lgkmcnt(0)
	s_setprio 1
	s_barrier
	v_mfma_f32_16x16x32_bf16 v[148:151], v[40:43], v[172:175], 0
	v_mfma_f32_16x16x32_bf16 v[144:147], v[80:83], v[172:175], 0
	v_mfma_f32_16x16x32_bf16 v[128:131], v[40:43], v[180:183], 0
	v_mfma_f32_16x16x32_bf16 v[124:127], v[80:83], v[180:183], 0
	v_mfma_f32_16x16x32_bf16 v[108:111], v[40:43], v[192:195], 0
	v_mfma_f32_16x16x32_bf16 v[104:107], v[80:83], v[192:195], 0
	v_mfma_f32_16x16x32_bf16 v[88:91], v[40:43], v[200:203], 0
	v_mfma_f32_16x16x32_bf16 v[84:87], v[80:83], v[200:203], 0
	v_mfma_f32_16x16x32_bf16 v[148:151], v[60:63], v[176:179], v[148:151]
	v_mfma_f32_16x16x32_bf16 v[144:147], v[100:103], v[176:179], v[144:147]
	v_mfma_f32_16x16x32_bf16 v[128:131], v[60:63], v[184:187], v[128:131]
	v_mfma_f32_16x16x32_bf16 v[124:127], v[100:103], v[184:187], v[124:127]
	v_mfma_f32_16x16x32_bf16 v[108:111], v[60:63], v[196:199], v[108:111]
	v_mfma_f32_16x16x32_bf16 v[104:107], v[100:103], v[196:199], v[104:107]
	v_mfma_f32_16x16x32_bf16 v[88:91], v[60:63], v[204:207], v[88:91]
	v_mfma_f32_16x16x32_bf16 v[84:87], v[100:103], v[204:207], v[84:87]
	s_setprio 0
	s_setprio 1
	v_mfma_f32_16x16x32_bf16 v[136:139], v[120:123], v[172:175], 0
	v_mfma_f32_16x16x32_bf16 v[132:135], v[152:155], v[172:175], 0
	v_mfma_f32_16x16x32_bf16 v[116:119], v[120:123], v[180:183], 0
	v_mfma_f32_16x16x32_bf16 v[112:115], v[152:155], v[180:183], 0
	v_mfma_f32_16x16x32_bf16 v[96:99], v[120:123], v[192:195], 0
	v_mfma_f32_16x16x32_bf16 v[92:95], v[152:155], v[192:195], 0
	v_mfma_f32_16x16x32_bf16 v[76:79], v[120:123], v[200:203], 0
	v_mfma_f32_16x16x32_bf16 v[72:75], v[152:155], v[200:203], 0
	v_mfma_f32_16x16x32_bf16 v[136:139], v[140:143], v[176:179], v[136:139]
	v_mfma_f32_16x16x32_bf16 v[132:135], v[156:159], v[176:179], v[132:135]
	v_mfma_f32_16x16x32_bf16 v[116:119], v[140:143], v[184:187], v[116:119]
	v_mfma_f32_16x16x32_bf16 v[112:115], v[156:159], v[184:187], v[112:115]
	v_mfma_f32_16x16x32_bf16 v[96:99], v[140:143], v[196:199], v[96:99]
	v_mfma_f32_16x16x32_bf16 v[92:95], v[156:159], v[196:199], v[92:95]
	v_mfma_f32_16x16x32_bf16 v[76:79], v[140:143], v[204:207], v[76:79]
	v_mfma_f32_16x16x32_bf16 v[72:75], v[156:159], v[204:207], v[72:75]
	s_barrier
	s_setprio 0
	s_mov_b32 m0, s23
	v_lshl_add_u64 v[188:189], s[24:25], 0, v[162:163]
	s_add_u32 s30, s24, 0x4000
	ds_read_b128 v[172:175], v191 offset:16384
	ds_read_b128 v[176:179], v191 offset:17408
	ds_read_b128 v[180:183], v191 offset:18432
	ds_read_b128 v[184:187], v191 offset:19456
	ds_read_b128 v[192:195], v191 offset:20480
	ds_read_b128 v[196:199], v191 offset:21504
	ds_read_b128 v[200:203], v191 offset:22528
	ds_read_b128 v[204:207], v191 offset:23552
	global_load_lds_dwordx4 v[188:189], off
	v_lshl_add_u64 v[188:189], s[24:25], 0, v[166:167]
	s_mov_b32 m0, s74
	s_addc_u32 s31, s25, 0
	global_load_lds_dwordx4 v[188:189], off
	v_lshl_add_u64 v[188:189], s[30:31], 0, v[162:163]
	s_mov_b32 m0, s76
	v_lshl_add_u64 v[208:209], s[38:39], 0, v[164:165]
	global_load_lds_dwordx4 v[188:189], off
	v_lshl_add_u64 v[188:189], s[30:31], 0, v[166:167]
	s_mov_b32 m0, s77
	s_nop 0
	global_load_lds_dwordx4 v[188:189], off
	v_lshl_add_u64 v[188:189], s[38:39], 0, v[160:161]
	s_mov_b32 m0, s78
	s_nop 0
	global_load_lds_dwordx4 v[188:189], off
	s_mov_b32 m0, s79
	s_nop 0
	global_load_lds_dwordx4 v[208:209], off
	s_waitcnt vmcnt(8)
	s_waitcnt lgkmcnt(0)
	s_setprio 1
	s_barrier
	v_mfma_f32_16x16x32_bf16 v[68:71], v[40:43], v[172:175], 0
	v_mfma_f32_16x16x32_bf16 v[64:67], v[80:83], v[172:175], 0
	v_mfma_f32_16x16x32_bf16 v[48:51], v[40:43], v[180:183], 0
	v_mfma_f32_16x16x32_bf16 v[44:47], v[80:83], v[180:183], 0
	v_mfma_f32_16x16x32_bf16 v[28:31], v[40:43], v[192:195], 0
	v_mfma_f32_16x16x32_bf16 v[24:27], v[80:83], v[192:195], 0
	v_mfma_f32_16x16x32_bf16 v[12:15], v[40:43], v[200:203], 0
	v_mfma_f32_16x16x32_bf16 v[8:11], v[80:83], v[200:203], 0
	v_mfma_f32_16x16x32_bf16 v[68:71], v[60:63], v[176:179], v[68:71]
	v_mfma_f32_16x16x32_bf16 v[64:67], v[100:103], v[176:179], v[64:67]
	v_mfma_f32_16x16x32_bf16 v[48:51], v[60:63], v[184:187], v[48:51]
	v_mfma_f32_16x16x32_bf16 v[44:47], v[100:103], v[184:187], v[44:47]
	v_mfma_f32_16x16x32_bf16 v[28:31], v[60:63], v[196:199], v[28:31]
	v_mfma_f32_16x16x32_bf16 v[24:27], v[100:103], v[196:199], v[24:27]
	v_mfma_f32_16x16x32_bf16 v[12:15], v[60:63], v[204:207], v[12:15]
	v_mfma_f32_16x16x32_bf16 v[8:11], v[100:103], v[204:207], v[8:11]
	s_setprio 0
	s_setprio 1
	v_mfma_f32_16x16x32_bf16 v[52:55], v[152:155], v[172:175], 0
	v_mfma_f32_16x16x32_bf16 v[36:39], v[120:123], v[180:183], 0
	v_mfma_f32_16x16x32_bf16 v[32:35], v[152:155], v[180:183], 0
	v_mfma_f32_16x16x32_bf16 v[20:23], v[120:123], v[192:195], 0
	v_mfma_f32_16x16x32_bf16 v[16:19], v[152:155], v[192:195], 0
	v_mfma_f32_16x16x32_bf16 v[4:7], v[120:123], v[200:203], 0
	v_mfma_f32_16x16x32_bf16 v[0:3], v[152:155], v[200:203], 0
	v_mfma_f32_16x16x32_bf16 v[40:43], v[120:123], v[172:175], 0
	v_mfma_f32_16x16x32_bf16 v[52:55], v[156:159], v[176:179], v[52:55]
	v_mfma_f32_16x16x32_bf16 v[36:39], v[140:143], v[184:187], v[36:39]
	v_mfma_f32_16x16x32_bf16 v[32:35], v[156:159], v[184:187], v[32:35]
	v_mfma_f32_16x16x32_bf16 v[20:23], v[140:143], v[196:199], v[20:23]
	v_mfma_f32_16x16x32_bf16 v[16:19], v[156:159], v[196:199], v[16:19]
	v_mfma_f32_16x16x32_bf16 v[4:7], v[140:143], v[204:207], v[4:7]
	v_mfma_f32_16x16x32_bf16 v[0:3], v[156:159], v[204:207], v[0:3]
	v_mfma_f32_16x16x32_bf16 v[40:43], v[140:143], v[176:179], v[40:43]
	s_barrier
	s_setprio 0
	v_add_u32_e32 v100, s86, v190
	v_add_u32_e32 v156, s95, v190
	ds_read_b128 v[56:59], v100
	ds_read_b128 v[60:63], v100 offset:1024
	ds_read_b128 v[80:83], v100 offset:2048
	ds_read_b128 v[100:103], v100 offset:3072
	ds_read_b128 v[120:123], v156
	ds_read_b128 v[140:143], v156 offset:1024
	ds_read_b128 v[152:155], v156 offset:2048
	ds_read_b128 v[156:159], v156 offset:3072
	s_add_u32 s30, s38, 0x80000
	s_addc_u32 s31, s39, 0
	s_mov_b32 m0, s82
	v_lshl_add_u64 v[210:211], s[30:31], 0, v[160:161]
	ds_read_b128 v[172:175], v191 offset:32768
	ds_read_b128 v[176:179], v191 offset:33792
	ds_read_b128 v[180:183], v191 offset:34816
	ds_read_b128 v[184:187], v191 offset:35840
	ds_read_b128 v[192:195], v191 offset:36864
	ds_read_b128 v[196:199], v191 offset:37888
	ds_read_b128 v[200:203], v191 offset:38912
	ds_read_b128 v[204:207], v191 offset:39936
	global_load_lds_dwordx4 v[210:211], off
	v_lshl_add_u64 v[210:211], s[30:31], 0, v[164:165]
	s_mov_b32 m0, s83
	s_nop 0
	global_load_lds_dwordx4 v[210:211], off
	s_waitcnt vmcnt(8)
	s_waitcnt lgkmcnt(0)
	s_setprio 1
	s_barrier
	v_mfma_f32_16x16x32_bf16 v[148:151], v[56:59], v[172:175], v[148:151]
	v_mfma_f32_16x16x32_bf16 v[144:147], v[80:83], v[172:175], v[144:147]
	v_mfma_f32_16x16x32_bf16 v[128:131], v[56:59], v[180:183], v[128:131]
	v_mfma_f32_16x16x32_bf16 v[124:127], v[80:83], v[180:183], v[124:127]
	v_mfma_f32_16x16x32_bf16 v[108:111], v[56:59], v[192:195], v[108:111]
	v_mfma_f32_16x16x32_bf16 v[104:107], v[80:83], v[192:195], v[104:107]
	v_mfma_f32_16x16x32_bf16 v[88:91], v[56:59], v[200:203], v[88:91]
	v_mfma_f32_16x16x32_bf16 v[84:87], v[80:83], v[200:203], v[84:87]
	v_mfma_f32_16x16x32_bf16 v[148:151], v[60:63], v[176:179], v[148:151]
	v_mfma_f32_16x16x32_bf16 v[144:147], v[100:103], v[176:179], v[144:147]
	v_mfma_f32_16x16x32_bf16 v[128:131], v[60:63], v[184:187], v[128:131]
	v_mfma_f32_16x16x32_bf16 v[124:127], v[100:103], v[184:187], v[124:127]
	v_mfma_f32_16x16x32_bf16 v[108:111], v[60:63], v[196:199], v[108:111]
	v_mfma_f32_16x16x32_bf16 v[104:107], v[100:103], v[196:199], v[104:107]
	v_mfma_f32_16x16x32_bf16 v[88:91], v[60:63], v[204:207], v[88:91]
	v_mfma_f32_16x16x32_bf16 v[84:87], v[100:103], v[204:207], v[84:87]
	s_setprio 0
	s_setprio 1
	v_mfma_f32_16x16x32_bf16 v[136:139], v[120:123], v[172:175], v[136:139]
	v_mfma_f32_16x16x32_bf16 v[132:135], v[152:155], v[172:175], v[132:135]
	v_mfma_f32_16x16x32_bf16 v[116:119], v[120:123], v[180:183], v[116:119]
	v_mfma_f32_16x16x32_bf16 v[112:115], v[152:155], v[180:183], v[112:115]
	v_mfma_f32_16x16x32_bf16 v[96:99], v[120:123], v[192:195], v[96:99]
	v_mfma_f32_16x16x32_bf16 v[92:95], v[152:155], v[192:195], v[92:95]
	v_mfma_f32_16x16x32_bf16 v[76:79], v[120:123], v[200:203], v[76:79]
	v_mfma_f32_16x16x32_bf16 v[72:75], v[152:155], v[200:203], v[72:75]
	v_mfma_f32_16x16x32_bf16 v[136:139], v[140:143], v[176:179], v[136:139]
	v_mfma_f32_16x16x32_bf16 v[132:135], v[156:159], v[176:179], v[132:135]
	v_mfma_f32_16x16x32_bf16 v[116:119], v[140:143], v[184:187], v[116:119]
	v_mfma_f32_16x16x32_bf16 v[112:115], v[156:159], v[184:187], v[112:115]
	v_mfma_f32_16x16x32_bf16 v[96:99], v[140:143], v[196:199], v[96:99]
	v_mfma_f32_16x16x32_bf16 v[92:95], v[156:159], v[196:199], v[92:95]
	v_mfma_f32_16x16x32_bf16 v[76:79], v[140:143], v[204:207], v[76:79]
	v_mfma_f32_16x16x32_bf16 v[72:75], v[156:159], v[204:207], v[72:75]
	s_barrier
	s_setprio 0
	s_add_u32 s30, s24, 0x8000
	s_addc_u32 s31, s25, 0
	s_mov_b32 m0, s87
	v_lshl_add_u64 v[210:211], s[30:31], 0, v[162:163]
	s_add_u32 s24, s24, 0xc000
	ds_read_b128 v[172:175], v191 offset:49152
	ds_read_b128 v[176:179], v191 offset:50176
	ds_read_b128 v[180:183], v191 offset:51200
	ds_read_b128 v[184:187], v191 offset:52224
	ds_read_b128 v[192:195], v191 offset:53248
	ds_read_b128 v[196:199], v191 offset:54272
	ds_read_b128 v[200:203], v191 offset:55296
	ds_read_b128 v[204:207], v191 offset:56320
	global_load_lds_dwordx4 v[210:211], off
	v_lshl_add_u64 v[210:211], s[30:31], 0, v[166:167]
	s_mov_b32 m0, s92
	s_addc_u32 s25, s25, 0
	global_load_lds_dwordx4 v[210:211], off
	v_lshl_add_u64 v[210:211], s[24:25], 0, v[162:163]
	s_mov_b32 m0, s96
	v_lshl_add_u64 v[188:189], v[188:189], 0, s[26:27]
	global_load_lds_dwordx4 v[210:211], off
	v_lshl_add_u64 v[210:211], s[24:25], 0, v[166:167]
	s_mov_b32 m0, s97
	s_nop 0
	global_load_lds_dwordx4 v[210:211], off
	s_mov_b32 m0, s93
	s_nop 0
	global_load_lds_dwordx4 v[188:189], off
	v_lshl_add_u64 v[188:189], v[208:209], 0, s[26:27]
	s_mov_b32 m0, s94
	s_nop 0
	global_load_lds_dwordx4 v[188:189], off
	s_waitcnt vmcnt(8)
	s_waitcnt lgkmcnt(0)
	s_setprio 1
	s_barrier
	v_mfma_f32_16x16x32_bf16 v[68:71], v[56:59], v[172:175], v[68:71]
	v_mfma_f32_16x16x32_bf16 v[64:67], v[80:83], v[172:175], v[64:67]
	v_mfma_f32_16x16x32_bf16 v[48:51], v[56:59], v[180:183], v[48:51]
	v_mfma_f32_16x16x32_bf16 v[44:47], v[80:83], v[180:183], v[44:47]
	v_mfma_f32_16x16x32_bf16 v[28:31], v[56:59], v[192:195], v[28:31]
	v_mfma_f32_16x16x32_bf16 v[24:27], v[80:83], v[192:195], v[24:27]
	v_mfma_f32_16x16x32_bf16 v[12:15], v[56:59], v[200:203], v[12:15]
	v_mfma_f32_16x16x32_bf16 v[8:11], v[80:83], v[200:203], v[8:11]
	v_mfma_f32_16x16x32_bf16 v[68:71], v[60:63], v[176:179], v[68:71]
	v_mfma_f32_16x16x32_bf16 v[64:67], v[100:103], v[176:179], v[64:67]
	v_mfma_f32_16x16x32_bf16 v[48:51], v[60:63], v[184:187], v[48:51]
	v_mfma_f32_16x16x32_bf16 v[44:47], v[100:103], v[184:187], v[44:47]
	v_mfma_f32_16x16x32_bf16 v[28:31], v[60:63], v[196:199], v[28:31]
	v_mfma_f32_16x16x32_bf16 v[24:27], v[100:103], v[196:199], v[24:27]
	v_mfma_f32_16x16x32_bf16 v[12:15], v[60:63], v[204:207], v[12:15]
	v_mfma_f32_16x16x32_bf16 v[8:11], v[100:103], v[204:207], v[8:11]
	s_setprio 0
	s_setprio 1
	v_mfma_f32_16x16x32_bf16 v[40:43], v[120:123], v[172:175], v[40:43]
	v_mfma_f32_16x16x32_bf16 v[56:59], v[140:143], v[176:179], v[40:43]
	v_mfma_f32_16x16x32_bf16 v[40:43], v[152:155], v[172:175], v[52:55]
	v_mfma_f32_16x16x32_bf16 v[36:39], v[120:123], v[180:183], v[36:39]
	v_mfma_f32_16x16x32_bf16 v[32:35], v[152:155], v[180:183], v[32:35]
	v_mfma_f32_16x16x32_bf16 v[20:23], v[120:123], v[192:195], v[20:23]
	v_mfma_f32_16x16x32_bf16 v[16:19], v[152:155], v[192:195], v[16:19]
	v_mfma_f32_16x16x32_bf16 v[4:7], v[120:123], v[200:203], v[4:7]
	v_mfma_f32_16x16x32_bf16 v[0:3], v[152:155], v[200:203], v[0:3]
	v_mfma_f32_16x16x32_bf16 v[52:55], v[156:159], v[176:179], v[40:43]
	v_mfma_f32_16x16x32_bf16 v[36:39], v[140:143], v[184:187], v[36:39]
	v_mfma_f32_16x16x32_bf16 v[32:35], v[156:159], v[184:187], v[32:35]
	v_mfma_f32_16x16x32_bf16 v[20:23], v[140:143], v[196:199], v[20:23]
	v_mfma_f32_16x16x32_bf16 v[16:19], v[156:159], v[196:199], v[16:19]
	v_mfma_f32_16x16x32_bf16 v[4:7], v[140:143], v[204:207], v[4:7]
	v_mfma_f32_16x16x32_bf16 v[0:3], v[156:159], v[204:207], v[0:3]
	s_barrier
	s_setprio 0
	s_add_i32 s28, s28, 2
	s_add_u32 s17, s17, 0x10000
	s_addc_u32 s19, s19, 0
	s_add_u32 s0, s0, 0x100
	s_addc_u32 s1, s1, 0
	s_cmp_gt_u32 s28, 29
.LBB0_311:
	v_add_u32_e32 v100, s3, v190
	v_add_u32_e32 v156, s75, v190
	ds_read_b128 v[40:43], v100
	ds_read_b128 v[60:63], v100 offset:1024
	ds_read_b128 v[80:83], v100 offset:2048
	ds_read_b128 v[100:103], v100 offset:3072
	ds_read_b128 v[120:123], v156
	ds_read_b128 v[140:143], v156 offset:1024
	ds_read_b128 v[152:155], v156 offset:2048
	ds_read_b128 v[156:159], v156 offset:3072
	s_add_u32 s24, s0, 0xfff80080
	s_addc_u32 s25, s1, -1
	s_cmp_eq_u32 s28, 28
	s_cselect_b32 s39, s4, s25
	s_cselect_b32 s38, s5, s24
	s_cselect_b32 s25, s8, s19
	s_cselect_b32 s24, s13, s17
	v_lshl_add_u64 v[188:189], s[0:1], 0, v[168:169]
	s_add_i32 m0, s78, 0xc000
	ds_read_b128 v[172:175], v191
	ds_read_b128 v[176:179], v191 offset:1024
	ds_read_b128 v[180:183], v191 offset:2048
	ds_read_b128 v[184:187], v191 offset:3072
	ds_read_b128 v[192:195], v191 offset:4096
	ds_read_b128 v[196:199], v191 offset:5120
	ds_read_b128 v[200:203], v191 offset:6144
	ds_read_b128 v[204:207], v191 offset:7168
	global_load_lds_dwordx4 v[188:189], off
	v_lshl_add_u64 v[188:189], s[0:1], 0, v[170:171]
	s_add_i32 m0, s78, 0xe000
	s_nop 0
	global_load_lds_dwordx4 v[188:189], off
	s_waitcnt vmcnt(8)
	s_waitcnt lgkmcnt(0)
	s_setprio 1
	s_barrier
	v_mfma_f32_16x16x32_bf16 v[148:151], v[40:43], v[172:175], v[148:151]
	v_mfma_f32_16x16x32_bf16 v[144:147], v[80:83], v[172:175], v[144:147]
	v_mfma_f32_16x16x32_bf16 v[128:131], v[40:43], v[180:183], v[128:131]
	v_mfma_f32_16x16x32_bf16 v[124:127], v[80:83], v[180:183], v[124:127]
	v_mfma_f32_16x16x32_bf16 v[108:111], v[40:43], v[192:195], v[108:111]
	v_mfma_f32_16x16x32_bf16 v[104:107], v[80:83], v[192:195], v[104:107]
	v_mfma_f32_16x16x32_bf16 v[88:91], v[40:43], v[200:203], v[88:91]
	v_mfma_f32_16x16x32_bf16 v[84:87], v[80:83], v[200:203], v[84:87]
	v_mfma_f32_16x16x32_bf16 v[148:151], v[60:63], v[176:179], v[148:151]
	v_mfma_f32_16x16x32_bf16 v[144:147], v[100:103], v[176:179], v[144:147]
	v_mfma_f32_16x16x32_bf16 v[128:131], v[60:63], v[184:187], v[128:131]
	v_mfma_f32_16x16x32_bf16 v[124:127], v[100:103], v[184:187], v[124:127]
	v_mfma_f32_16x16x32_bf16 v[108:111], v[60:63], v[196:199], v[108:111]
	v_mfma_f32_16x16x32_bf16 v[104:107], v[100:103], v[196:199], v[104:107]
	v_mfma_f32_16x16x32_bf16 v[88:91], v[60:63], v[204:207], v[88:91]
	v_mfma_f32_16x16x32_bf16 v[84:87], v[100:103], v[204:207], v[84:87]
	s_setprio 0
	s_setprio 1
	v_mfma_f32_16x16x32_bf16 v[136:139], v[120:123], v[172:175], v[136:139]
	v_mfma_f32_16x16x32_bf16 v[132:135], v[152:155], v[172:175], v[132:135]
	v_mfma_f32_16x16x32_bf16 v[116:119], v[120:123], v[180:183], v[116:119]
	v_mfma_f32_16x16x32_bf16 v[112:115], v[152:155], v[180:183], v[112:115]
	v_mfma_f32_16x16x32_bf16 v[96:99], v[120:123], v[192:195], v[96:99]
	v_mfma_f32_16x16x32_bf16 v[92:95], v[152:155], v[192:195], v[92:95]
	v_mfma_f32_16x16x32_bf16 v[76:79], v[120:123], v[200:203], v[76:79]
	v_mfma_f32_16x16x32_bf16 v[72:75], v[152:155], v[200:203], v[72:75]
	v_mfma_f32_16x16x32_bf16 v[136:139], v[140:143], v[176:179], v[136:139]
	v_mfma_f32_16x16x32_bf16 v[132:135], v[156:159], v[176:179], v[132:135]
	v_mfma_f32_16x16x32_bf16 v[116:119], v[140:143], v[184:187], v[116:119]
	v_mfma_f32_16x16x32_bf16 v[112:115], v[156:159], v[184:187], v[112:115]
	v_mfma_f32_16x16x32_bf16 v[96:99], v[140:143], v[196:199], v[96:99]
	v_mfma_f32_16x16x32_bf16 v[92:95], v[156:159], v[196:199], v[92:95]
	v_mfma_f32_16x16x32_bf16 v[76:79], v[140:143], v[204:207], v[76:79]
	v_mfma_f32_16x16x32_bf16 v[72:75], v[156:159], v[204:207], v[72:75]
	s_barrier
	s_setprio 0
	s_mov_b32 m0, s23
	v_lshl_add_u64 v[188:189], s[24:25], 0, v[162:163]
	s_add_u32 s30, s24, 0x4000
	ds_read_b128 v[172:175], v191 offset:16384
	ds_read_b128 v[176:179], v191 offset:17408
	ds_read_b128 v[180:183], v191 offset:18432
	ds_read_b128 v[184:187], v191 offset:19456
	ds_read_b128 v[192:195], v191 offset:20480
	ds_read_b128 v[196:199], v191 offset:21504
	ds_read_b128 v[200:203], v191 offset:22528
	ds_read_b128 v[204:207], v191 offset:23552
	global_load_lds_dwordx4 v[188:189], off
	v_lshl_add_u64 v[188:189], s[24:25], 0, v[166:167]
	s_mov_b32 m0, s74
	s_addc_u32 s31, s25, 0
	global_load_lds_dwordx4 v[188:189], off
	v_lshl_add_u64 v[188:189], s[30:31], 0, v[162:163]
	s_mov_b32 m0, s76
	v_lshl_add_u64 v[208:209], s[38:39], 0, v[164:165]
	global_load_lds_dwordx4 v[188:189], off
	v_lshl_add_u64 v[188:189], s[30:31], 0, v[166:167]
	s_mov_b32 m0, s77
	s_nop 0
	global_load_lds_dwordx4 v[188:189], off
	v_lshl_add_u64 v[188:189], s[38:39], 0, v[160:161]
	s_mov_b32 m0, s78
	s_nop 0
	global_load_lds_dwordx4 v[188:189], off
	s_mov_b32 m0, s79
	s_nop 0
	global_load_lds_dwordx4 v[208:209], off
	s_waitcnt vmcnt(8)
	s_waitcnt lgkmcnt(0)
	s_setprio 1
	s_barrier
	v_mfma_f32_16x16x32_bf16 v[68:71], v[40:43], v[172:175], v[68:71]
	v_mfma_f32_16x16x32_bf16 v[64:67], v[80:83], v[172:175], v[64:67]
	v_mfma_f32_16x16x32_bf16 v[48:51], v[40:43], v[180:183], v[48:51]
	v_mfma_f32_16x16x32_bf16 v[44:47], v[80:83], v[180:183], v[44:47]
	v_mfma_f32_16x16x32_bf16 v[28:31], v[40:43], v[192:195], v[28:31]
	v_mfma_f32_16x16x32_bf16 v[24:27], v[80:83], v[192:195], v[24:27]
	v_mfma_f32_16x16x32_bf16 v[12:15], v[40:43], v[200:203], v[12:15]
	v_mfma_f32_16x16x32_bf16 v[8:11], v[80:83], v[200:203], v[8:11]
	v_mfma_f32_16x16x32_bf16 v[68:71], v[60:63], v[176:179], v[68:71]
	v_mfma_f32_16x16x32_bf16 v[64:67], v[100:103], v[176:179], v[64:67]
	v_mfma_f32_16x16x32_bf16 v[48:51], v[60:63], v[184:187], v[48:51]
	v_mfma_f32_16x16x32_bf16 v[44:47], v[100:103], v[184:187], v[44:47]
	v_mfma_f32_16x16x32_bf16 v[28:31], v[60:63], v[196:199], v[28:31]
	v_mfma_f32_16x16x32_bf16 v[24:27], v[100:103], v[196:199], v[24:27]
	v_mfma_f32_16x16x32_bf16 v[12:15], v[60:63], v[204:207], v[12:15]
	v_mfma_f32_16x16x32_bf16 v[8:11], v[100:103], v[204:207], v[8:11]
	s_setprio 0
	s_setprio 1
	v_mfma_f32_16x16x32_bf16 v[52:55], v[152:155], v[172:175], v[52:55]
	v_mfma_f32_16x16x32_bf16 v[36:39], v[120:123], v[180:183], v[36:39]
	v_mfma_f32_16x16x32_bf16 v[32:35], v[152:155], v[180:183], v[32:35]
	v_mfma_f32_16x16x32_bf16 v[20:23], v[120:123], v[192:195], v[20:23]
	v_mfma_f32_16x16x32_bf16 v[16:19], v[152:155], v[192:195], v[16:19]
	v_mfma_f32_16x16x32_bf16 v[4:7], v[120:123], v[200:203], v[4:7]
	v_mfma_f32_16x16x32_bf16 v[0:3], v[152:155], v[200:203], v[0:3]
	v_mfma_f32_16x16x32_bf16 v[40:43], v[120:123], v[172:175], v[56:59]
	v_mfma_f32_16x16x32_bf16 v[52:55], v[156:159], v[176:179], v[52:55]
	v_mfma_f32_16x16x32_bf16 v[36:39], v[140:143], v[184:187], v[36:39]
	v_mfma_f32_16x16x32_bf16 v[32:35], v[156:159], v[184:187], v[32:35]
	v_mfma_f32_16x16x32_bf16 v[20:23], v[140:143], v[196:199], v[20:23]
	v_mfma_f32_16x16x32_bf16 v[16:19], v[156:159], v[196:199], v[16:19]
	v_mfma_f32_16x16x32_bf16 v[4:7], v[140:143], v[204:207], v[4:7]
	v_mfma_f32_16x16x32_bf16 v[0:3], v[156:159], v[204:207], v[0:3]
	v_mfma_f32_16x16x32_bf16 v[40:43], v[140:143], v[176:179], v[40:43]
	s_barrier
	s_setprio 0
	v_add_u32_e32 v100, s86, v190
	v_add_u32_e32 v156, s95, v190
	ds_read_b128 v[56:59], v100
	ds_read_b128 v[60:63], v100 offset:1024
	ds_read_b128 v[80:83], v100 offset:2048
	ds_read_b128 v[100:103], v100 offset:3072
	ds_read_b128 v[120:123], v156
	ds_read_b128 v[140:143], v156 offset:1024
	ds_read_b128 v[152:155], v156 offset:2048
	ds_read_b128 v[156:159], v156 offset:3072
	s_add_u32 s30, s38, 0x80000
	s_addc_u32 s31, s39, 0
	s_mov_b32 m0, s82
	v_lshl_add_u64 v[210:211], s[30:31], 0, v[160:161]
	ds_read_b128 v[172:175], v191 offset:32768
	ds_read_b128 v[176:179], v191 offset:33792
	ds_read_b128 v[180:183], v191 offset:34816
	ds_read_b128 v[184:187], v191 offset:35840
	ds_read_b128 v[192:195], v191 offset:36864
	ds_read_b128 v[196:199], v191 offset:37888
	ds_read_b128 v[200:203], v191 offset:38912
	ds_read_b128 v[204:207], v191 offset:39936
	global_load_lds_dwordx4 v[210:211], off
	v_lshl_add_u64 v[210:211], s[30:31], 0, v[164:165]
	s_mov_b32 m0, s83
	s_nop 0
	global_load_lds_dwordx4 v[210:211], off
	s_waitcnt vmcnt(8)
	s_waitcnt lgkmcnt(0)
	s_setprio 1
	s_barrier
	v_mfma_f32_16x16x32_bf16 v[148:151], v[56:59], v[172:175], v[148:151]
	v_mfma_f32_16x16x32_bf16 v[144:147], v[80:83], v[172:175], v[144:147]
	v_mfma_f32_16x16x32_bf16 v[128:131], v[56:59], v[180:183], v[128:131]
	v_mfma_f32_16x16x32_bf16 v[124:127], v[80:83], v[180:183], v[124:127]
	v_mfma_f32_16x16x32_bf16 v[108:111], v[56:59], v[192:195], v[108:111]
	v_mfma_f32_16x16x32_bf16 v[104:107], v[80:83], v[192:195], v[104:107]
	v_mfma_f32_16x16x32_bf16 v[88:91], v[56:59], v[200:203], v[88:91]
	v_mfma_f32_16x16x32_bf16 v[84:87], v[80:83], v[200:203], v[84:87]
	v_mfma_f32_16x16x32_bf16 v[148:151], v[60:63], v[176:179], v[148:151]
	v_mfma_f32_16x16x32_bf16 v[144:147], v[100:103], v[176:179], v[144:147]
	v_mfma_f32_16x16x32_bf16 v[128:131], v[60:63], v[184:187], v[128:131]
	v_mfma_f32_16x16x32_bf16 v[124:127], v[100:103], v[184:187], v[124:127]
	v_mfma_f32_16x16x32_bf16 v[108:111], v[60:63], v[196:199], v[108:111]
	v_mfma_f32_16x16x32_bf16 v[104:107], v[100:103], v[196:199], v[104:107]
	v_mfma_f32_16x16x32_bf16 v[88:91], v[60:63], v[204:207], v[88:91]
	v_mfma_f32_16x16x32_bf16 v[84:87], v[100:103], v[204:207], v[84:87]
	s_setprio 0
	s_setprio 1
	v_mfma_f32_16x16x32_bf16 v[136:139], v[120:123], v[172:175], v[136:139]
	v_mfma_f32_16x16x32_bf16 v[132:135], v[152:155], v[172:175], v[132:135]
	v_mfma_f32_16x16x32_bf16 v[116:119], v[120:123], v[180:183], v[116:119]
	v_mfma_f32_16x16x32_bf16 v[112:115], v[152:155], v[180:183], v[112:115]
	v_mfma_f32_16x16x32_bf16 v[96:99], v[120:123], v[192:195], v[96:99]
	v_mfma_f32_16x16x32_bf16 v[92:95], v[152:155], v[192:195], v[92:95]
	v_mfma_f32_16x16x32_bf16 v[76:79], v[120:123], v[200:203], v[76:79]
	v_mfma_f32_16x16x32_bf16 v[72:75], v[152:155], v[200:203], v[72:75]
	v_mfma_f32_16x16x32_bf16 v[136:139], v[140:143], v[176:179], v[136:139]
	v_mfma_f32_16x16x32_bf16 v[132:135], v[156:159], v[176:179], v[132:135]
	v_mfma_f32_16x16x32_bf16 v[116:119], v[140:143], v[184:187], v[116:119]
	v_mfma_f32_16x16x32_bf16 v[112:115], v[156:159], v[184:187], v[112:115]
	v_mfma_f32_16x16x32_bf16 v[96:99], v[140:143], v[196:199], v[96:99]
	v_mfma_f32_16x16x32_bf16 v[92:95], v[156:159], v[196:199], v[92:95]
	v_mfma_f32_16x16x32_bf16 v[76:79], v[140:143], v[204:207], v[76:79]
	v_mfma_f32_16x16x32_bf16 v[72:75], v[156:159], v[204:207], v[72:75]
	s_barrier
	s_setprio 0
	s_add_u32 s30, s24, 0x8000
	s_addc_u32 s31, s25, 0
	s_mov_b32 m0, s87
	v_lshl_add_u64 v[210:211], s[30:31], 0, v[162:163]
	s_add_u32 s24, s24, 0xc000
	ds_read_b128 v[172:175], v191 offset:49152
	ds_read_b128 v[176:179], v191 offset:50176
	ds_read_b128 v[180:183], v191 offset:51200
	ds_read_b128 v[184:187], v191 offset:52224
	ds_read_b128 v[192:195], v191 offset:53248
	ds_read_b128 v[196:199], v191 offset:54272
	ds_read_b128 v[200:203], v191 offset:55296
	ds_read_b128 v[204:207], v191 offset:56320
	global_load_lds_dwordx4 v[210:211], off
	v_lshl_add_u64 v[210:211], s[30:31], 0, v[166:167]
	s_mov_b32 m0, s92
	s_addc_u32 s25, s25, 0
	global_load_lds_dwordx4 v[210:211], off
	v_lshl_add_u64 v[210:211], s[24:25], 0, v[162:163]
	s_mov_b32 m0, s96
	v_lshl_add_u64 v[188:189], v[188:189], 0, s[26:27]
	global_load_lds_dwordx4 v[210:211], off
	v_lshl_add_u64 v[210:211], s[24:25], 0, v[166:167]
	s_mov_b32 m0, s97
	s_nop 0
	global_load_lds_dwordx4 v[210:211], off
	s_mov_b32 m0, s93
	s_nop 0
	global_load_lds_dwordx4 v[188:189], off
	v_lshl_add_u64 v[188:189], v[208:209], 0, s[26:27]
	s_mov_b32 m0, s94
	s_nop 0
	global_load_lds_dwordx4 v[188:189], off
	s_waitcnt vmcnt(8)
	s_waitcnt lgkmcnt(0)
	s_setprio 1
	s_barrier
	v_mfma_f32_16x16x32_bf16 v[68:71], v[56:59], v[172:175], v[68:71]
	v_mfma_f32_16x16x32_bf16 v[64:67], v[80:83], v[172:175], v[64:67]
	v_mfma_f32_16x16x32_bf16 v[48:51], v[56:59], v[180:183], v[48:51]
	v_mfma_f32_16x16x32_bf16 v[44:47], v[80:83], v[180:183], v[44:47]
	v_mfma_f32_16x16x32_bf16 v[28:31], v[56:59], v[192:195], v[28:31]
	v_mfma_f32_16x16x32_bf16 v[24:27], v[80:83], v[192:195], v[24:27]
	v_mfma_f32_16x16x32_bf16 v[12:15], v[56:59], v[200:203], v[12:15]
	v_mfma_f32_16x16x32_bf16 v[8:11], v[80:83], v[200:203], v[8:11]
	v_mfma_f32_16x16x32_bf16 v[68:71], v[60:63], v[176:179], v[68:71]
	v_mfma_f32_16x16x32_bf16 v[64:67], v[100:103], v[176:179], v[64:67]
	v_mfma_f32_16x16x32_bf16 v[48:51], v[60:63], v[184:187], v[48:51]
	v_mfma_f32_16x16x32_bf16 v[44:47], v[100:103], v[184:187], v[44:47]
	v_mfma_f32_16x16x32_bf16 v[28:31], v[60:63], v[196:199], v[28:31]
	v_mfma_f32_16x16x32_bf16 v[24:27], v[100:103], v[196:199], v[24:27]
	v_mfma_f32_16x16x32_bf16 v[12:15], v[60:63], v[204:207], v[12:15]
	v_mfma_f32_16x16x32_bf16 v[8:11], v[100:103], v[204:207], v[8:11]
	s_setprio 0
	s_setprio 1
	v_mfma_f32_16x16x32_bf16 v[40:43], v[120:123], v[172:175], v[40:43]
	v_mfma_f32_16x16x32_bf16 v[56:59], v[140:143], v[176:179], v[40:43]
	v_mfma_f32_16x16x32_bf16 v[40:43], v[152:155], v[172:175], v[52:55]
	v_mfma_f32_16x16x32_bf16 v[36:39], v[120:123], v[180:183], v[36:39]
	v_mfma_f32_16x16x32_bf16 v[32:35], v[152:155], v[180:183], v[32:35]
	v_mfma_f32_16x16x32_bf16 v[20:23], v[120:123], v[192:195], v[20:23]
	v_mfma_f32_16x16x32_bf16 v[16:19], v[152:155], v[192:195], v[16:19]
	v_mfma_f32_16x16x32_bf16 v[4:7], v[120:123], v[200:203], v[4:7]
	v_mfma_f32_16x16x32_bf16 v[0:3], v[152:155], v[200:203], v[0:3]
	v_mfma_f32_16x16x32_bf16 v[52:55], v[156:159], v[176:179], v[40:43]
	v_mfma_f32_16x16x32_bf16 v[36:39], v[140:143], v[184:187], v[36:39]
	v_mfma_f32_16x16x32_bf16 v[32:35], v[156:159], v[184:187], v[32:35]
	v_mfma_f32_16x16x32_bf16 v[20:23], v[140:143], v[196:199], v[20:23]
	v_mfma_f32_16x16x32_bf16 v[16:19], v[156:159], v[196:199], v[16:19]
	v_mfma_f32_16x16x32_bf16 v[4:7], v[140:143], v[204:207], v[4:7]
	v_mfma_f32_16x16x32_bf16 v[0:3], v[156:159], v[204:207], v[0:3]
	s_barrier
	s_setprio 0
	s_add_i32 s28, s28, 2
	s_add_u32 s17, s17, 0x10000
	s_addc_u32 s19, s19, 0
	s_add_u32 s0, s0, 0x100
	s_addc_u32 s1, s1, 0
	s_cmp_gt_u32 s28, 29
	s_cbranch_scc0 .LBB0_311
	s_and_b64 vcc, exec, s[34:35]
	s_cbranch_vccz .LBB0_314
	s_barrier

.LBB0_1054:
	s_ashr_i32 s41, s40, 31
	s_lshl_b64 s[4:5], s[40:41], 20
	s_add_u32 s44, s16, s4
	s_addc_u32 s45, s17, s5
	s_and_b64 s[4:5], s[36:37], exec
	s_cselect_b32 s4, s45, s51
	s_cselect_b32 s5, s44, s50
	s_ashr_i32 s39, s38, 31
	s_lshl_b64 s[46:47], s[38:39], 20
	s_add_u32 s46, s18, s46
	s_addc_u32 s47, s19, s47
	s_and_b64 s[52:53], s[36:37], exec
	s_cselect_b32 s39, s47, s1
	s_cselect_b32 s41, s46, s0
	s_add_u32 s49, s0, 0x10000
	s_addc_u32 s55, s1, 0
	s_add_u32 s0, s50, 0x80080
	s_addc_u32 s1, s51, 0
	s_mov_b32 s80, -2
	v_add_u32_e32 v140, s28, v215
	v_add_u32_e32 v156, s54, v215
	ds_read_b128 v[128:131], v140
	ds_read_b128 v[132:135], v140 offset:1024
	ds_read_b128 v[136:139], v140 offset:2048
	ds_read_b128 v[140:143], v140 offset:3072
	ds_read_b128 v[144:147], v156
	ds_read_b128 v[148:151], v156 offset:1024
	ds_read_b128 v[152:155], v156 offset:2048
	ds_read_b128 v[156:159], v156 offset:3072
	s_add_u32 s50, s0, 0xfff80080
	s_addc_u32 s51, s1, -1
	s_cmp_eq_u32 s80, 28
	s_cselect_b32 s53, s4, s51
	s_cselect_b32 s52, s5, s50
	s_cselect_b32 s51, s39, s55
	s_cselect_b32 s50, s41, s49
	v_lshl_add_u64 v[204:205], s[0:1], 0, v[180:181]
	s_add_i32 m0, s58, 0xc000
	ds_read_b128 v[160:163], v251
	ds_read_b128 v[164:167], v251 offset:1024
	ds_read_b128 v[168:171], v251 offset:2048
	ds_read_b128 v[184:187], v251 offset:3072
	ds_read_b128 v[188:191], v251 offset:4096
	ds_read_b128 v[192:195], v251 offset:5120
	ds_read_b128 v[196:199], v251 offset:6144
	ds_read_b128 v[200:203], v251 offset:7168
	global_load_lds_dwordx4 v[204:205], off
	v_lshl_add_u64 v[204:205], s[0:1], 0, v[182:183]
	s_add_i32 m0, s58, 0xe000
	s_nop 0
	global_load_lds_dwordx4 v[204:205], off
	s_waitcnt vmcnt(8)
	s_waitcnt lgkmcnt(0)
	s_setprio 1
	s_barrier
	v_mfma_f32_16x16x32_bf16 v[124:127], v[128:131], v[160:163], 0
	v_mfma_f32_16x16x32_bf16 v[120:123], v[136:139], v[160:163], 0
	v_mfma_f32_16x16x32_bf16 v[116:119], v[128:131], v[168:171], 0
	v_mfma_f32_16x16x32_bf16 v[112:115], v[136:139], v[168:171], 0
	v_mfma_f32_16x16x32_bf16 v[108:111], v[128:131], v[188:191], 0
	v_mfma_f32_16x16x32_bf16 v[104:107], v[136:139], v[188:191], 0
	v_mfma_f32_16x16x32_bf16 v[100:103], v[128:131], v[196:199], 0
	v_mfma_f32_16x16x32_bf16 v[96:99], v[136:139], v[196:199], 0
	v_mfma_f32_16x16x32_bf16 v[124:127], v[132:135], v[164:167], v[124:127]
	v_mfma_f32_16x16x32_bf16 v[120:123], v[140:143], v[164:167], v[120:123]
	v_mfma_f32_16x16x32_bf16 v[116:119], v[132:135], v[184:187], v[116:119]
	v_mfma_f32_16x16x32_bf16 v[112:115], v[140:143], v[184:187], v[112:115]
	v_mfma_f32_16x16x32_bf16 v[108:111], v[132:135], v[192:195], v[108:111]
	v_mfma_f32_16x16x32_bf16 v[104:107], v[140:143], v[192:195], v[104:107]
	v_mfma_f32_16x16x32_bf16 v[100:103], v[132:135], v[200:203], v[100:103]
	v_mfma_f32_16x16x32_bf16 v[96:99], v[140:143], v[200:203], v[96:99]
	s_setprio 0
	s_setprio 1
	v_mfma_f32_16x16x32_bf16 v[60:63], v[144:147], v[160:163], 0
	v_mfma_f32_16x16x32_bf16 v[56:59], v[152:155], v[160:163], 0
	v_mfma_f32_16x16x32_bf16 v[52:55], v[144:147], v[168:171], 0
	v_mfma_f32_16x16x32_bf16 v[48:51], v[152:155], v[168:171], 0
	v_mfma_f32_16x16x32_bf16 v[44:47], v[144:147], v[188:191], 0
	v_mfma_f32_16x16x32_bf16 v[40:43], v[152:155], v[188:191], 0
	v_mfma_f32_16x16x32_bf16 v[36:39], v[144:147], v[196:199], 0
	v_mfma_f32_16x16x32_bf16 v[32:35], v[152:155], v[196:199], 0
	v_mfma_f32_16x16x32_bf16 v[60:63], v[148:151], v[164:167], v[60:63]
	v_mfma_f32_16x16x32_bf16 v[56:59], v[156:159], v[164:167], v[56:59]
	v_mfma_f32_16x16x32_bf16 v[52:55], v[148:151], v[184:187], v[52:55]
	v_mfma_f32_16x16x32_bf16 v[48:51], v[156:159], v[184:187], v[48:51]
	v_mfma_f32_16x16x32_bf16 v[44:47], v[148:151], v[192:195], v[44:47]
	v_mfma_f32_16x16x32_bf16 v[40:43], v[156:159], v[192:195], v[40:43]
	v_mfma_f32_16x16x32_bf16 v[36:39], v[148:151], v[200:203], v[36:39]
	v_mfma_f32_16x16x32_bf16 v[32:35], v[156:159], v[200:203], v[32:35]
	s_barrier
	s_setprio 0
	s_mov_b32 m0, s30
	v_lshl_add_u64 v[204:205], s[50:51], 0, v[174:175]
	s_add_u32 s82, s50, 0x4000
	ds_read_b128 v[160:163], v251 offset:16384
	ds_read_b128 v[164:167], v251 offset:17408
	ds_read_b128 v[168:171], v251 offset:18432
	ds_read_b128 v[184:187], v251 offset:19456
	ds_read_b128 v[188:191], v251 offset:20480
	ds_read_b128 v[192:195], v251 offset:21504
	ds_read_b128 v[196:199], v251 offset:22528
	ds_read_b128 v[200:203], v251 offset:23552
	global_load_lds_dwordx4 v[204:205], off
	v_lshl_add_u64 v[204:205], s[50:51], 0, v[178:179]
	s_mov_b32 m0, s43
	s_addc_u32 s83, s51, 0
	global_load_lds_dwordx4 v[204:205], off
	v_lshl_add_u64 v[204:205], s[82:83], 0, v[174:175]
	s_mov_b32 m0, s56
	v_lshl_add_u64 v[206:207], s[52:53], 0, v[176:177]
	global_load_lds_dwordx4 v[204:205], off
	v_lshl_add_u64 v[204:205], s[82:83], 0, v[178:179]
	s_mov_b32 m0, s57
	s_nop 0
	global_load_lds_dwordx4 v[204:205], off
	v_lshl_add_u64 v[204:205], s[52:53], 0, v[172:173]
	s_mov_b32 m0, s58
	s_nop 0
	global_load_lds_dwordx4 v[204:205], off
	s_mov_b32 m0, s59
	s_nop 0
	global_load_lds_dwordx4 v[206:207], off
	s_waitcnt vmcnt(8)
	s_waitcnt lgkmcnt(0)
	s_setprio 1
	s_barrier
	v_mfma_f32_16x16x32_bf16 v[92:95], v[128:131], v[160:163], 0
	v_mfma_f32_16x16x32_bf16 v[88:91], v[136:139], v[160:163], 0
	v_mfma_f32_16x16x32_bf16 v[84:87], v[128:131], v[168:171], 0
	v_mfma_f32_16x16x32_bf16 v[80:83], v[136:139], v[168:171], 0
	v_mfma_f32_16x16x32_bf16 v[76:79], v[128:131], v[188:191], 0
	v_mfma_f32_16x16x32_bf16 v[72:75], v[136:139], v[188:191], 0
	v_mfma_f32_16x16x32_bf16 v[68:71], v[128:131], v[196:199], 0
	v_mfma_f32_16x16x32_bf16 v[64:67], v[136:139], v[196:199], 0
	v_mfma_f32_16x16x32_bf16 v[92:95], v[132:135], v[164:167], v[92:95]
	v_mfma_f32_16x16x32_bf16 v[88:91], v[140:143], v[164:167], v[88:91]
	v_mfma_f32_16x16x32_bf16 v[84:87], v[132:135], v[184:187], v[84:87]
	v_mfma_f32_16x16x32_bf16 v[80:83], v[140:143], v[184:187], v[80:83]
	v_mfma_f32_16x16x32_bf16 v[76:79], v[132:135], v[192:195], v[76:79]
	v_mfma_f32_16x16x32_bf16 v[72:75], v[140:143], v[192:195], v[72:75]
	v_mfma_f32_16x16x32_bf16 v[68:71], v[132:135], v[200:203], v[68:71]
	v_mfma_f32_16x16x32_bf16 v[64:67], v[140:143], v[200:203], v[64:67]
	s_setprio 0
	s_setprio 1
	v_mfma_f32_16x16x32_bf16 v[28:31], v[144:147], v[160:163], 0
	v_mfma_f32_16x16x32_bf16 v[24:27], v[152:155], v[160:163], 0
	v_mfma_f32_16x16x32_bf16 v[20:23], v[144:147], v[168:171], 0
	v_mfma_f32_16x16x32_bf16 v[16:19], v[152:155], v[168:171], 0
	v_mfma_f32_16x16x32_bf16 v[12:15], v[144:147], v[188:191], 0
	v_mfma_f32_16x16x32_bf16 v[8:11], v[152:155], v[188:191], 0
	v_mfma_f32_16x16x32_bf16 v[4:7], v[144:147], v[196:199], 0
	v_mfma_f32_16x16x32_bf16 v[0:3], v[152:155], v[196:199], 0
	v_mfma_f32_16x16x32_bf16 v[28:31], v[148:151], v[164:167], v[28:31]
	v_mfma_f32_16x16x32_bf16 v[24:27], v[156:159], v[164:167], v[24:27]
	v_mfma_f32_16x16x32_bf16 v[20:23], v[148:151], v[184:187], v[20:23]
	v_mfma_f32_16x16x32_bf16 v[16:19], v[156:159], v[184:187], v[16:19]
	v_mfma_f32_16x16x32_bf16 v[12:15], v[148:151], v[192:195], v[12:15]
	v_mfma_f32_16x16x32_bf16 v[8:11], v[156:159], v[192:195], v[8:11]
	v_mfma_f32_16x16x32_bf16 v[4:7], v[148:151], v[200:203], v[4:7]
	v_mfma_f32_16x16x32_bf16 v[0:3], v[156:159], v[200:203], v[0:3]
	s_barrier
	s_setprio 0
	v_add_u32_e32 v140, s68, v215
	v_add_u32_e32 v156, s73, v215
	ds_read_b128 v[128:131], v140
	ds_read_b128 v[132:135], v140 offset:1024
	ds_read_b128 v[136:139], v140 offset:2048
	ds_read_b128 v[140:143], v140 offset:3072
	ds_read_b128 v[144:147], v156
	ds_read_b128 v[148:151], v156 offset:1024
	ds_read_b128 v[152:155], v156 offset:2048
	ds_read_b128 v[156:159], v156 offset:3072
	s_add_u32 s52, s52, 0x80000
	s_addc_u32 s53, s53, 0
	s_mov_b32 m0, s60
	v_lshl_add_u64 v[208:209], s[52:53], 0, v[172:173]
	ds_read_b128 v[160:163], v251 offset:32768
	ds_read_b128 v[164:167], v251 offset:33792
	ds_read_b128 v[168:171], v251 offset:34816
	ds_read_b128 v[184:187], v251 offset:35840
	ds_read_b128 v[188:191], v251 offset:36864
	ds_read_b128 v[192:195], v251 offset:37888
	ds_read_b128 v[196:199], v251 offset:38912
	ds_read_b128 v[200:203], v251 offset:39936
	global_load_lds_dwordx4 v[208:209], off
	v_lshl_add_u64 v[208:209], s[52:53], 0, v[176:177]
	s_mov_b32 m0, s61
	s_nop 0
	global_load_lds_dwordx4 v[208:209], off
	s_waitcnt vmcnt(8)
	s_waitcnt lgkmcnt(0)
	s_setprio 1
	s_barrier
	v_mfma_f32_16x16x32_bf16 v[124:127], v[128:131], v[160:163], v[124:127]
	v_mfma_f32_16x16x32_bf16 v[120:123], v[136:139], v[160:163], v[120:123]
	v_mfma_f32_16x16x32_bf16 v[116:119], v[128:131], v[168:171], v[116:119]
	v_mfma_f32_16x16x32_bf16 v[112:115], v[136:139], v[168:171], v[112:115]
	v_mfma_f32_16x16x32_bf16 v[108:111], v[128:131], v[188:191], v[108:111]
	v_mfma_f32_16x16x32_bf16 v[104:107], v[136:139], v[188:191], v[104:107]
	v_mfma_f32_16x16x32_bf16 v[100:103], v[128:131], v[196:199], v[100:103]
	v_mfma_f32_16x16x32_bf16 v[96:99], v[136:139], v[196:199], v[96:99]
	v_mfma_f32_16x16x32_bf16 v[124:127], v[132:135], v[164:167], v[124:127]
	v_mfma_f32_16x16x32_bf16 v[120:123], v[140:143], v[164:167], v[120:123]
	v_mfma_f32_16x16x32_bf16 v[116:119], v[132:135], v[184:187], v[116:119]
	v_mfma_f32_16x16x32_bf16 v[112:115], v[140:143], v[184:187], v[112:115]
	v_mfma_f32_16x16x32_bf16 v[108:111], v[132:135], v[192:195], v[108:111]
	v_mfma_f32_16x16x32_bf16 v[104:107], v[140:143], v[192:195], v[104:107]
	v_mfma_f32_16x16x32_bf16 v[100:103], v[132:135], v[200:203], v[100:103]
	v_mfma_f32_16x16x32_bf16 v[96:99], v[140:143], v[200:203], v[96:99]
	s_setprio 0
	s_setprio 1
	v_mfma_f32_16x16x32_bf16 v[60:63], v[144:147], v[160:163], v[60:63]
	v_mfma_f32_16x16x32_bf16 v[56:59], v[152:155], v[160:163], v[56:59]
	v_mfma_f32_16x16x32_bf16 v[52:55], v[144:147], v[168:171], v[52:55]
	v_mfma_f32_16x16x32_bf16 v[48:51], v[152:155], v[168:171], v[48:51]
	v_mfma_f32_16x16x32_bf16 v[44:47], v[144:147], v[188:191], v[44:47]
	v_mfma_f32_16x16x32_bf16 v[40:43], v[152:155], v[188:191], v[40:43]
	v_mfma_f32_16x16x32_bf16 v[36:39], v[144:147], v[196:199], v[36:39]
	v_mfma_f32_16x16x32_bf16 v[32:35], v[152:155], v[196:199], v[32:35]
	v_mfma_f32_16x16x32_bf16 v[60:63], v[148:151], v[164:167], v[60:63]
	v_mfma_f32_16x16x32_bf16 v[56:59], v[156:159], v[164:167], v[56:59]
	v_mfma_f32_16x16x32_bf16 v[52:55], v[148:151], v[184:187], v[52:55]
	v_mfma_f32_16x16x32_bf16 v[48:51], v[156:159], v[184:187], v[48:51]
	v_mfma_f32_16x16x32_bf16 v[44:47], v[148:151], v[192:195], v[44:47]
	v_mfma_f32_16x16x32_bf16 v[40:43], v[156:159], v[192:195], v[40:43]
	v_mfma_f32_16x16x32_bf16 v[36:39], v[148:151], v[200:203], v[36:39]
	v_mfma_f32_16x16x32_bf16 v[32:35], v[156:159], v[200:203], v[32:35]
	s_barrier
	s_setprio 0
	s_add_u32 s52, s50, 0x8000
	s_addc_u32 s53, s51, 0
	s_mov_b32 m0, s69
	v_lshl_add_u64 v[208:209], s[52:53], 0, v[174:175]
	s_add_u32 s50, s50, 0xc000
	ds_read_b128 v[160:163], v251 offset:49152
	ds_read_b128 v[164:167], v251 offset:50176
	ds_read_b128 v[168:171], v251 offset:51200
	ds_read_b128 v[184:187], v251 offset:52224
	ds_read_b128 v[188:191], v251 offset:53248
	ds_read_b128 v[192:195], v251 offset:54272
	ds_read_b128 v[196:199], v251 offset:55296
	ds_read_b128 v[200:203], v251 offset:56320
	global_load_lds_dwordx4 v[208:209], off
	v_lshl_add_u64 v[208:209], s[52:53], 0, v[178:179]
	s_mov_b32 m0, s70
	s_addc_u32 s51, s51, 0
	global_load_lds_dwordx4 v[208:209], off
	v_lshl_add_u64 v[208:209], s[50:51], 0, v[174:175]
	s_mov_b32 m0, s74
	v_lshl_add_u64 v[204:205], v[204:205], 0, s[26:27]
	global_load_lds_dwordx4 v[208:209], off
	v_lshl_add_u64 v[208:209], s[50:51], 0, v[178:179]
	s_mov_b32 m0, s75
	s_nop 0
	global_load_lds_dwordx4 v[208:209], off
	s_mov_b32 m0, s71
	s_nop 0
	global_load_lds_dwordx4 v[204:205], off
	v_lshl_add_u64 v[204:205], v[206:207], 0, s[26:27]
	s_mov_b32 m0, s72
	s_nop 0
	global_load_lds_dwordx4 v[204:205], off
	s_waitcnt vmcnt(8)
	s_waitcnt lgkmcnt(0)
	s_setprio 1
	s_barrier
	v_mfma_f32_16x16x32_bf16 v[92:95], v[128:131], v[160:163], v[92:95]
	v_mfma_f32_16x16x32_bf16 v[88:91], v[136:139], v[160:163], v[88:91]
	v_mfma_f32_16x16x32_bf16 v[84:87], v[128:131], v[168:171], v[84:87]
	v_mfma_f32_16x16x32_bf16 v[80:83], v[136:139], v[168:171], v[80:83]
	v_mfma_f32_16x16x32_bf16 v[76:79], v[128:131], v[188:191], v[76:79]
	v_mfma_f32_16x16x32_bf16 v[72:75], v[136:139], v[188:191], v[72:75]
	v_mfma_f32_16x16x32_bf16 v[68:71], v[128:131], v[196:199], v[68:71]
	v_mfma_f32_16x16x32_bf16 v[64:67], v[136:139], v[196:199], v[64:67]
	v_mfma_f32_16x16x32_bf16 v[92:95], v[132:135], v[164:167], v[92:95]
	v_mfma_f32_16x16x32_bf16 v[88:91], v[140:143], v[164:167], v[88:91]
	v_mfma_f32_16x16x32_bf16 v[84:87], v[132:135], v[184:187], v[84:87]
	v_mfma_f32_16x16x32_bf16 v[80:83], v[140:143], v[184:187], v[80:83]
	v_mfma_f32_16x16x32_bf16 v[76:79], v[132:135], v[192:195], v[76:79]
	v_mfma_f32_16x16x32_bf16 v[72:75], v[140:143], v[192:195], v[72:75]
	v_mfma_f32_16x16x32_bf16 v[68:71], v[132:135], v[200:203], v[68:71]
	v_mfma_f32_16x16x32_bf16 v[64:67], v[140:143], v[200:203], v[64:67]
	s_setprio 0
	s_setprio 1
	v_mfma_f32_16x16x32_bf16 v[28:31], v[144:147], v[160:163], v[28:31]
	v_mfma_f32_16x16x32_bf16 v[24:27], v[152:155], v[160:163], v[24:27]
	v_mfma_f32_16x16x32_bf16 v[20:23], v[144:147], v[168:171], v[20:23]
	v_mfma_f32_16x16x32_bf16 v[16:19], v[152:155], v[168:171], v[16:19]
	v_mfma_f32_16x16x32_bf16 v[12:15], v[144:147], v[188:191], v[12:15]
	v_mfma_f32_16x16x32_bf16 v[8:11], v[152:155], v[188:191], v[8:11]
	v_mfma_f32_16x16x32_bf16 v[4:7], v[144:147], v[196:199], v[4:7]
	v_mfma_f32_16x16x32_bf16 v[0:3], v[152:155], v[196:199], v[0:3]
	v_mfma_f32_16x16x32_bf16 v[28:31], v[148:151], v[164:167], v[28:31]
	v_mfma_f32_16x16x32_bf16 v[24:27], v[156:159], v[164:167], v[24:27]
	v_mfma_f32_16x16x32_bf16 v[20:23], v[148:151], v[184:187], v[20:23]
	v_mfma_f32_16x16x32_bf16 v[16:19], v[156:159], v[184:187], v[16:19]
	v_mfma_f32_16x16x32_bf16 v[12:15], v[148:151], v[192:195], v[12:15]
	v_mfma_f32_16x16x32_bf16 v[8:11], v[156:159], v[192:195], v[8:11]
	v_mfma_f32_16x16x32_bf16 v[4:7], v[148:151], v[200:203], v[4:7]
	v_mfma_f32_16x16x32_bf16 v[0:3], v[156:159], v[200:203], v[0:3]
	s_barrier
	s_setprio 0
	s_add_i32 s80, s80, 2
	s_add_u32 s49, s49, 0x10000
	s_addc_u32 s55, s55, 0
	s_add_u32 s0, s0, 0x100
	s_addc_u32 s1, s1, 0
	s_cmp_gt_u32 s80, 29
.LBB0_1055:
	v_add_u32_e32 v140, s28, v215
	v_add_u32_e32 v156, s54, v215
	ds_read_b128 v[128:131], v140
	ds_read_b128 v[132:135], v140 offset:1024
	ds_read_b128 v[136:139], v140 offset:2048
	ds_read_b128 v[140:143], v140 offset:3072
	ds_read_b128 v[144:147], v156
	ds_read_b128 v[148:151], v156 offset:1024
	ds_read_b128 v[152:155], v156 offset:2048
	ds_read_b128 v[156:159], v156 offset:3072
	s_add_u32 s50, s0, 0xfff80080
	s_addc_u32 s51, s1, -1
	s_cmp_eq_u32 s80, 28
	s_cselect_b32 s53, s4, s51
	s_cselect_b32 s52, s5, s50
	s_cselect_b32 s51, s39, s55
	s_cselect_b32 s50, s41, s49
	v_lshl_add_u64 v[204:205], s[0:1], 0, v[180:181]
	s_add_i32 m0, s58, 0xc000
	ds_read_b128 v[160:163], v251
	ds_read_b128 v[164:167], v251 offset:1024
	ds_read_b128 v[168:171], v251 offset:2048
	ds_read_b128 v[184:187], v251 offset:3072
	ds_read_b128 v[188:191], v251 offset:4096
	ds_read_b128 v[192:195], v251 offset:5120
	ds_read_b128 v[196:199], v251 offset:6144
	ds_read_b128 v[200:203], v251 offset:7168
	global_load_lds_dwordx4 v[204:205], off
	v_lshl_add_u64 v[204:205], s[0:1], 0, v[182:183]
	s_add_i32 m0, s58, 0xe000
	s_nop 0
	global_load_lds_dwordx4 v[204:205], off
	s_waitcnt vmcnt(8)
	s_waitcnt lgkmcnt(0)
	s_setprio 1
	s_barrier
	v_mfma_f32_16x16x32_bf16 v[124:127], v[128:131], v[160:163], v[124:127]
	v_mfma_f32_16x16x32_bf16 v[120:123], v[136:139], v[160:163], v[120:123]
	v_mfma_f32_16x16x32_bf16 v[116:119], v[128:131], v[168:171], v[116:119]
	v_mfma_f32_16x16x32_bf16 v[112:115], v[136:139], v[168:171], v[112:115]
	v_mfma_f32_16x16x32_bf16 v[108:111], v[128:131], v[188:191], v[108:111]
	v_mfma_f32_16x16x32_bf16 v[104:107], v[136:139], v[188:191], v[104:107]
	v_mfma_f32_16x16x32_bf16 v[100:103], v[128:131], v[196:199], v[100:103]
	v_mfma_f32_16x16x32_bf16 v[96:99], v[136:139], v[196:199], v[96:99]
	v_mfma_f32_16x16x32_bf16 v[124:127], v[132:135], v[164:167], v[124:127]
	v_mfma_f32_16x16x32_bf16 v[120:123], v[140:143], v[164:167], v[120:123]
	v_mfma_f32_16x16x32_bf16 v[116:119], v[132:135], v[184:187], v[116:119]
	v_mfma_f32_16x16x32_bf16 v[112:115], v[140:143], v[184:187], v[112:115]
	v_mfma_f32_16x16x32_bf16 v[108:111], v[132:135], v[192:195], v[108:111]
	v_mfma_f32_16x16x32_bf16 v[104:107], v[140:143], v[192:195], v[104:107]
	v_mfma_f32_16x16x32_bf16 v[100:103], v[132:135], v[200:203], v[100:103]
	v_mfma_f32_16x16x32_bf16 v[96:99], v[140:143], v[200:203], v[96:99]
	s_setprio 0
	s_setprio 1
	v_mfma_f32_16x16x32_bf16 v[60:63], v[144:147], v[160:163], v[60:63]
	v_mfma_f32_16x16x32_bf16 v[56:59], v[152:155], v[160:163], v[56:59]
	v_mfma_f32_16x16x32_bf16 v[52:55], v[144:147], v[168:171], v[52:55]
	v_mfma_f32_16x16x32_bf16 v[48:51], v[152:155], v[168:171], v[48:51]
	v_mfma_f32_16x16x32_bf16 v[44:47], v[144:147], v[188:191], v[44:47]
	v_mfma_f32_16x16x32_bf16 v[40:43], v[152:155], v[188:191], v[40:43]
	v_mfma_f32_16x16x32_bf16 v[36:39], v[144:147], v[196:199], v[36:39]
	v_mfma_f32_16x16x32_bf16 v[32:35], v[152:155], v[196:199], v[32:35]
	v_mfma_f32_16x16x32_bf16 v[60:63], v[148:151], v[164:167], v[60:63]
	v_mfma_f32_16x16x32_bf16 v[56:59], v[156:159], v[164:167], v[56:59]
	v_mfma_f32_16x16x32_bf16 v[52:55], v[148:151], v[184:187], v[52:55]
	v_mfma_f32_16x16x32_bf16 v[48:51], v[156:159], v[184:187], v[48:51]
	v_mfma_f32_16x16x32_bf16 v[44:47], v[148:151], v[192:195], v[44:47]
	v_mfma_f32_16x16x32_bf16 v[40:43], v[156:159], v[192:195], v[40:43]
	v_mfma_f32_16x16x32_bf16 v[36:39], v[148:151], v[200:203], v[36:39]
	v_mfma_f32_16x16x32_bf16 v[32:35], v[156:159], v[200:203], v[32:35]
	s_barrier
	s_setprio 0
	s_mov_b32 m0, s30
	v_lshl_add_u64 v[204:205], s[50:51], 0, v[174:175]
	s_add_u32 s82, s50, 0x4000
	ds_read_b128 v[160:163], v251 offset:16384
	ds_read_b128 v[164:167], v251 offset:17408
	ds_read_b128 v[168:171], v251 offset:18432
	ds_read_b128 v[184:187], v251 offset:19456
	ds_read_b128 v[188:191], v251 offset:20480
	ds_read_b128 v[192:195], v251 offset:21504
	ds_read_b128 v[196:199], v251 offset:22528
	ds_read_b128 v[200:203], v251 offset:23552
	global_load_lds_dwordx4 v[204:205], off
	v_lshl_add_u64 v[204:205], s[50:51], 0, v[178:179]
	s_mov_b32 m0, s43
	s_addc_u32 s83, s51, 0
	global_load_lds_dwordx4 v[204:205], off
	v_lshl_add_u64 v[204:205], s[82:83], 0, v[174:175]
	s_mov_b32 m0, s56
	v_lshl_add_u64 v[206:207], s[52:53], 0, v[176:177]
	global_load_lds_dwordx4 v[204:205], off
	v_lshl_add_u64 v[204:205], s[82:83], 0, v[178:179]
	s_mov_b32 m0, s57
	s_nop 0
	global_load_lds_dwordx4 v[204:205], off
	v_lshl_add_u64 v[204:205], s[52:53], 0, v[172:173]
	s_mov_b32 m0, s58
	s_nop 0
	global_load_lds_dwordx4 v[204:205], off
	s_mov_b32 m0, s59
	s_nop 0
	global_load_lds_dwordx4 v[206:207], off
	s_waitcnt vmcnt(8)
	s_waitcnt lgkmcnt(0)
	s_setprio 1
	s_barrier
	v_mfma_f32_16x16x32_bf16 v[92:95], v[128:131], v[160:163], v[92:95]
	v_mfma_f32_16x16x32_bf16 v[88:91], v[136:139], v[160:163], v[88:91]
	v_mfma_f32_16x16x32_bf16 v[84:87], v[128:131], v[168:171], v[84:87]
	v_mfma_f32_16x16x32_bf16 v[80:83], v[136:139], v[168:171], v[80:83]
	v_mfma_f32_16x16x32_bf16 v[76:79], v[128:131], v[188:191], v[76:79]
	v_mfma_f32_16x16x32_bf16 v[72:75], v[136:139], v[188:191], v[72:75]
	v_mfma_f32_16x16x32_bf16 v[68:71], v[128:131], v[196:199], v[68:71]
	v_mfma_f32_16x16x32_bf16 v[64:67], v[136:139], v[196:199], v[64:67]
	v_mfma_f32_16x16x32_bf16 v[92:95], v[132:135], v[164:167], v[92:95]
	v_mfma_f32_16x16x32_bf16 v[88:91], v[140:143], v[164:167], v[88:91]
	v_mfma_f32_16x16x32_bf16 v[84:87], v[132:135], v[184:187], v[84:87]
	v_mfma_f32_16x16x32_bf16 v[80:83], v[140:143], v[184:187], v[80:83]
	v_mfma_f32_16x16x32_bf16 v[76:79], v[132:135], v[192:195], v[76:79]
	v_mfma_f32_16x16x32_bf16 v[72:75], v[140:143], v[192:195], v[72:75]
	v_mfma_f32_16x16x32_bf16 v[68:71], v[132:135], v[200:203], v[68:71]
	v_mfma_f32_16x16x32_bf16 v[64:67], v[140:143], v[200:203], v[64:67]
	s_setprio 0
	s_setprio 1
	v_mfma_f32_16x16x32_bf16 v[28:31], v[144:147], v[160:163], v[28:31]
	v_mfma_f32_16x16x32_bf16 v[24:27], v[152:155], v[160:163], v[24:27]
	v_mfma_f32_16x16x32_bf16 v[20:23], v[144:147], v[168:171], v[20:23]
	v_mfma_f32_16x16x32_bf16 v[16:19], v[152:155], v[168:171], v[16:19]
	v_mfma_f32_16x16x32_bf16 v[12:15], v[144:147], v[188:191], v[12:15]
	v_mfma_f32_16x16x32_bf16 v[8:11], v[152:155], v[188:191], v[8:11]
	v_mfma_f32_16x16x32_bf16 v[4:7], v[144:147], v[196:199], v[4:7]
	v_mfma_f32_16x16x32_bf16 v[0:3], v[152:155], v[196:199], v[0:3]
	v_mfma_f32_16x16x32_bf16 v[28:31], v[148:151], v[164:167], v[28:31]
	v_mfma_f32_16x16x32_bf16 v[24:27], v[156:159], v[164:167], v[24:27]
	v_mfma_f32_16x16x32_bf16 v[20:23], v[148:151], v[184:187], v[20:23]
	v_mfma_f32_16x16x32_bf16 v[16:19], v[156:159], v[184:187], v[16:19]
	v_mfma_f32_16x16x32_bf16 v[12:15], v[148:151], v[192:195], v[12:15]
	v_mfma_f32_16x16x32_bf16 v[8:11], v[156:159], v[192:195], v[8:11]
	v_mfma_f32_16x16x32_bf16 v[4:7], v[148:151], v[200:203], v[4:7]
	v_mfma_f32_16x16x32_bf16 v[0:3], v[156:159], v[200:203], v[0:3]
	s_barrier
	s_setprio 0
	v_add_u32_e32 v140, s68, v215
	v_add_u32_e32 v156, s73, v215
	ds_read_b128 v[128:131], v140
	ds_read_b128 v[132:135], v140 offset:1024
	ds_read_b128 v[136:139], v140 offset:2048
	ds_read_b128 v[140:143], v140 offset:3072
	ds_read_b128 v[144:147], v156
	ds_read_b128 v[148:151], v156 offset:1024
	ds_read_b128 v[152:155], v156 offset:2048
	ds_read_b128 v[156:159], v156 offset:3072
	s_add_u32 s52, s52, 0x80000
	s_addc_u32 s53, s53, 0
	s_mov_b32 m0, s60
	v_lshl_add_u64 v[208:209], s[52:53], 0, v[172:173]
	ds_read_b128 v[160:163], v251 offset:32768
	ds_read_b128 v[164:167], v251 offset:33792
	ds_read_b128 v[168:171], v251 offset:34816
	ds_read_b128 v[184:187], v251 offset:35840
	ds_read_b128 v[188:191], v251 offset:36864
	ds_read_b128 v[192:195], v251 offset:37888
	ds_read_b128 v[196:199], v251 offset:38912
	ds_read_b128 v[200:203], v251 offset:39936
	global_load_lds_dwordx4 v[208:209], off
	v_lshl_add_u64 v[208:209], s[52:53], 0, v[176:177]
	s_mov_b32 m0, s61
	s_nop 0
	global_load_lds_dwordx4 v[208:209], off
	s_waitcnt vmcnt(8)
	s_waitcnt lgkmcnt(0)
	s_setprio 1
	s_barrier
	v_mfma_f32_16x16x32_bf16 v[124:127], v[128:131], v[160:163], v[124:127]
	v_mfma_f32_16x16x32_bf16 v[120:123], v[136:139], v[160:163], v[120:123]
	v_mfma_f32_16x16x32_bf16 v[116:119], v[128:131], v[168:171], v[116:119]
	v_mfma_f32_16x16x32_bf16 v[112:115], v[136:139], v[168:171], v[112:115]
	v_mfma_f32_16x16x32_bf16 v[108:111], v[128:131], v[188:191], v[108:111]
	v_mfma_f32_16x16x32_bf16 v[104:107], v[136:139], v[188:191], v[104:107]
	v_mfma_f32_16x16x32_bf16 v[100:103], v[128:131], v[196:199], v[100:103]
	v_mfma_f32_16x16x32_bf16 v[96:99], v[136:139], v[196:199], v[96:99]
	v_mfma_f32_16x16x32_bf16 v[124:127], v[132:135], v[164:167], v[124:127]
	v_mfma_f32_16x16x32_bf16 v[120:123], v[140:143], v[164:167], v[120:123]
	v_mfma_f32_16x16x32_bf16 v[116:119], v[132:135], v[184:187], v[116:119]
	v_mfma_f32_16x16x32_bf16 v[112:115], v[140:143], v[184:187], v[112:115]
	v_mfma_f32_16x16x32_bf16 v[108:111], v[132:135], v[192:195], v[108:111]
	v_mfma_f32_16x16x32_bf16 v[104:107], v[140:143], v[192:195], v[104:107]
	v_mfma_f32_16x16x32_bf16 v[100:103], v[132:135], v[200:203], v[100:103]
	v_mfma_f32_16x16x32_bf16 v[96:99], v[140:143], v[200:203], v[96:99]
	s_setprio 0
	s_setprio 1
	v_mfma_f32_16x16x32_bf16 v[60:63], v[144:147], v[160:163], v[60:63]
	v_mfma_f32_16x16x32_bf16 v[56:59], v[152:155], v[160:163], v[56:59]
	v_mfma_f32_16x16x32_bf16 v[52:55], v[144:147], v[168:171], v[52:55]
	v_mfma_f32_16x16x32_bf16 v[48:51], v[152:155], v[168:171], v[48:51]
	v_mfma_f32_16x16x32_bf16 v[44:47], v[144:147], v[188:191], v[44:47]
	v_mfma_f32_16x16x32_bf16 v[40:43], v[152:155], v[188:191], v[40:43]
	v_mfma_f32_16x16x32_bf16 v[36:39], v[144:147], v[196:199], v[36:39]
	v_mfma_f32_16x16x32_bf16 v[32:35], v[152:155], v[196:199], v[32:35]
	v_mfma_f32_16x16x32_bf16 v[60:63], v[148:151], v[164:167], v[60:63]
	v_mfma_f32_16x16x32_bf16 v[56:59], v[156:159], v[164:167], v[56:59]
	v_mfma_f32_16x16x32_bf16 v[52:55], v[148:151], v[184:187], v[52:55]
	v_mfma_f32_16x16x32_bf16 v[48:51], v[156:159], v[184:187], v[48:51]
	v_mfma_f32_16x16x32_bf16 v[44:47], v[148:151], v[192:195], v[44:47]
	v_mfma_f32_16x16x32_bf16 v[40:43], v[156:159], v[192:195], v[40:43]
	v_mfma_f32_16x16x32_bf16 v[36:39], v[148:151], v[200:203], v[36:39]
	v_mfma_f32_16x16x32_bf16 v[32:35], v[156:159], v[200:203], v[32:35]
	s_barrier
	s_setprio 0
	s_add_u32 s52, s50, 0x8000
	s_addc_u32 s53, s51, 0
	s_mov_b32 m0, s69
	v_lshl_add_u64 v[208:209], s[52:53], 0, v[174:175]
	s_add_u32 s50, s50, 0xc000
	ds_read_b128 v[160:163], v251 offset:49152
	ds_read_b128 v[164:167], v251 offset:50176
	ds_read_b128 v[168:171], v251 offset:51200
	ds_read_b128 v[184:187], v251 offset:52224
	ds_read_b128 v[188:191], v251 offset:53248
	ds_read_b128 v[192:195], v251 offset:54272
	ds_read_b128 v[196:199], v251 offset:55296
	ds_read_b128 v[200:203], v251 offset:56320
	global_load_lds_dwordx4 v[208:209], off
	v_lshl_add_u64 v[208:209], s[52:53], 0, v[178:179]
	s_mov_b32 m0, s70
	s_addc_u32 s51, s51, 0
	global_load_lds_dwordx4 v[208:209], off
	v_lshl_add_u64 v[208:209], s[50:51], 0, v[174:175]
	s_mov_b32 m0, s74
	v_lshl_add_u64 v[204:205], v[204:205], 0, s[26:27]
	global_load_lds_dwordx4 v[208:209], off
	v_lshl_add_u64 v[208:209], s[50:51], 0, v[178:179]
	s_mov_b32 m0, s75
	s_nop 0
	global_load_lds_dwordx4 v[208:209], off
	s_mov_b32 m0, s71
	s_nop 0
	global_load_lds_dwordx4 v[204:205], off
	v_lshl_add_u64 v[204:205], v[206:207], 0, s[26:27]
	s_mov_b32 m0, s72
	s_nop 0
	global_load_lds_dwordx4 v[204:205], off
	s_waitcnt vmcnt(8)
	s_waitcnt lgkmcnt(0)
	s_setprio 1
	s_barrier
	v_mfma_f32_16x16x32_bf16 v[92:95], v[128:131], v[160:163], v[92:95]
	v_mfma_f32_16x16x32_bf16 v[88:91], v[136:139], v[160:163], v[88:91]
	v_mfma_f32_16x16x32_bf16 v[84:87], v[128:131], v[168:171], v[84:87]
	v_mfma_f32_16x16x32_bf16 v[80:83], v[136:139], v[168:171], v[80:83]
	v_mfma_f32_16x16x32_bf16 v[76:79], v[128:131], v[188:191], v[76:79]
	v_mfma_f32_16x16x32_bf16 v[72:75], v[136:139], v[188:191], v[72:75]
	v_mfma_f32_16x16x32_bf16 v[68:71], v[128:131], v[196:199], v[68:71]
	v_mfma_f32_16x16x32_bf16 v[64:67], v[136:139], v[196:199], v[64:67]
	v_mfma_f32_16x16x32_bf16 v[92:95], v[132:135], v[164:167], v[92:95]
	v_mfma_f32_16x16x32_bf16 v[88:91], v[140:143], v[164:167], v[88:91]
	v_mfma_f32_16x16x32_bf16 v[84:87], v[132:135], v[184:187], v[84:87]
	v_mfma_f32_16x16x32_bf16 v[80:83], v[140:143], v[184:187], v[80:83]
	v_mfma_f32_16x16x32_bf16 v[76:79], v[132:135], v[192:195], v[76:79]
	v_mfma_f32_16x16x32_bf16 v[72:75], v[140:143], v[192:195], v[72:75]
	v_mfma_f32_16x16x32_bf16 v[68:71], v[132:135], v[200:203], v[68:71]
	v_mfma_f32_16x16x32_bf16 v[64:67], v[140:143], v[200:203], v[64:67]
	s_setprio 0
	s_setprio 1
	v_mfma_f32_16x16x32_bf16 v[28:31], v[144:147], v[160:163], v[28:31]
	v_mfma_f32_16x16x32_bf16 v[24:27], v[152:155], v[160:163], v[24:27]
	v_mfma_f32_16x16x32_bf16 v[20:23], v[144:147], v[168:171], v[20:23]
	v_mfma_f32_16x16x32_bf16 v[16:19], v[152:155], v[168:171], v[16:19]
	v_mfma_f32_16x16x32_bf16 v[12:15], v[144:147], v[188:191], v[12:15]
	v_mfma_f32_16x16x32_bf16 v[8:11], v[152:155], v[188:191], v[8:11]
	v_mfma_f32_16x16x32_bf16 v[4:7], v[144:147], v[196:199], v[4:7]
	v_mfma_f32_16x16x32_bf16 v[0:3], v[152:155], v[196:199], v[0:3]
	v_mfma_f32_16x16x32_bf16 v[28:31], v[148:151], v[164:167], v[28:31]
	v_mfma_f32_16x16x32_bf16 v[24:27], v[156:159], v[164:167], v[24:27]
	v_mfma_f32_16x16x32_bf16 v[20:23], v[148:151], v[184:187], v[20:23]
	v_mfma_f32_16x16x32_bf16 v[16:19], v[156:159], v[184:187], v[16:19]
	v_mfma_f32_16x16x32_bf16 v[12:15], v[148:151], v[192:195], v[12:15]
	v_mfma_f32_16x16x32_bf16 v[8:11], v[156:159], v[192:195], v[8:11]
	v_mfma_f32_16x16x32_bf16 v[4:7], v[148:151], v[200:203], v[4:7]
	v_mfma_f32_16x16x32_bf16 v[0:3], v[156:159], v[200:203], v[0:3]
	s_barrier
	s_setprio 0
	s_add_i32 s80, s80, 2
	s_add_u32 s49, s49, 0x10000
	s_addc_u32 s55, s55, 0
	s_add_u32 s0, s0, 0x100
	s_addc_u32 s1, s1, 0
	s_cmp_gt_u32 s80, 29
	s_cbranch_scc0 .LBB0_1055
	v_mov_b64_e32 v[220:221], 0x1ff
	v_mov_b64_e32 v[218:219], 0x200
	s_and_b64 vcc, exec, s[34:35]
	s_cbranch_vccz .LBB0_1058
	s_barrier

.LBB0_1172:
	s_ashr_i32 s39, s38, 31
	s_lshl_b64 s[4:5], s[38:39], 20
	s_add_u32 s40, s18, s4
	s_addc_u32 s41, s19, s5
	s_and_b64 s[4:5], s[36:37], exec
	s_cselect_b32 s4, s41, s1
	s_cselect_b32 s5, s40, s0
	s_ashr_i32 s35, s34, 31
	s_lshl_b64 s[42:43], s[34:35], 20
	s_add_u32 s42, s16, s42
	s_addc_u32 s43, s17, s43
	s_and_b64 s[48:49], s[36:37], exec
	s_cselect_b32 s35, s43, s47
	s_cselect_b32 s39, s42, s46
	s_add_u32 s76, s46, 0x10000
	s_addc_u32 s77, s47, 0
	s_mov_b32 s78, -2
	v_add_u32_e32 v124, s28, v156
	v_add_u32_e32 v170, s45, v156
	ds_read_b128 v[108:111], v124
	ds_read_b128 v[112:115], v124 offset:1024
	ds_read_b128 v[120:123], v124 offset:2048
	ds_read_b128 v[124:127], v124 offset:3072
	ds_read_b128 v[158:161], v170
	ds_read_b128 v[162:165], v170 offset:1024
	ds_read_b128 v[166:169], v170 offset:2048
	ds_read_b128 v[170:173], v170 offset:3072
	s_add_u32 s46, s0, 0x10000
	s_addc_u32 s47, s1, 0
	s_cmp_eq_u32 s78, 28
	s_cselect_b32 s52, s5, s46
	s_cselect_b32 s53, s4, s47
	s_cselect_b32 s50, s39, s76
	s_cselect_b32 s51, s35, s77
	s_add_u32 s48, s52, 0x8000
	s_addc_u32 s49, s53, 0
	v_lshl_add_u64 v[206:207], s[0:1], 0, v[152:153]
	s_add_i32 m0, s56, 0xc000
	ds_read_b128 v[174:177], v157
	ds_read_b128 v[178:181], v157 offset:1024
	ds_read_b128 v[182:185], v157 offset:2048
	ds_read_b128 v[186:189], v157 offset:3072
	ds_read_b128 v[190:193], v157 offset:4096
	ds_read_b128 v[194:197], v157 offset:5120
	ds_read_b128 v[198:201], v157 offset:6144
	ds_read_b128 v[202:205], v157 offset:7168
	global_load_lds_dwordx4 v[206:207], off
	v_lshl_add_u64 v[206:207], s[0:1], 0, v[154:155]
	s_add_i32 m0, s56, 0xe000
	s_nop 0
	global_load_lds_dwordx4 v[206:207], off
	s_waitcnt vmcnt(8)
	s_waitcnt lgkmcnt(0)
	s_setprio 1
	s_barrier
	v_mfma_f32_16x16x32_bf16 v[140:143], v[108:111], v[174:177], 0
	v_mfma_f32_16x16x32_bf16 v[136:139], v[120:123], v[174:177], 0
	v_mfma_f32_16x16x32_bf16 v[116:119], v[108:111], v[182:185], 0
	v_mfma_f32_16x16x32_bf16 v[104:107], v[120:123], v[182:185], 0
	v_mfma_f32_16x16x32_bf16 v[92:95], v[108:111], v[190:193], 0
	v_mfma_f32_16x16x32_bf16 v[88:91], v[120:123], v[190:193], 0
	v_mfma_f32_16x16x32_bf16 v[76:79], v[108:111], v[198:201], 0
	v_mfma_f32_16x16x32_bf16 v[72:75], v[120:123], v[198:201], 0
	v_mfma_f32_16x16x32_bf16 v[140:143], v[112:115], v[178:181], v[140:143]
	v_mfma_f32_16x16x32_bf16 v[136:139], v[124:127], v[178:181], v[136:139]
	v_mfma_f32_16x16x32_bf16 v[116:119], v[112:115], v[186:189], v[116:119]
	v_mfma_f32_16x16x32_bf16 v[104:107], v[124:127], v[186:189], v[104:107]
	v_mfma_f32_16x16x32_bf16 v[92:95], v[112:115], v[194:197], v[92:95]
	v_mfma_f32_16x16x32_bf16 v[88:91], v[124:127], v[194:197], v[88:91]
	v_mfma_f32_16x16x32_bf16 v[76:79], v[112:115], v[202:205], v[76:79]
	v_mfma_f32_16x16x32_bf16 v[72:75], v[124:127], v[202:205], v[72:75]
	s_setprio 0
	s_setprio 1
	v_mfma_f32_16x16x32_bf16 v[132:135], v[158:161], v[174:177], 0
	v_mfma_f32_16x16x32_bf16 v[128:131], v[166:169], v[174:177], 0
	v_mfma_f32_16x16x32_bf16 v[100:103], v[158:161], v[182:185], 0
	v_mfma_f32_16x16x32_bf16 v[96:99], v[166:169], v[182:185], 0
	v_mfma_f32_16x16x32_bf16 v[84:87], v[158:161], v[190:193], 0
	v_mfma_f32_16x16x32_bf16 v[80:83], v[166:169], v[190:193], 0
	v_mfma_f32_16x16x32_bf16 v[68:71], v[158:161], v[198:201], 0
	v_mfma_f32_16x16x32_bf16 v[64:67], v[166:169], v[198:201], 0
	v_mfma_f32_16x16x32_bf16 v[132:135], v[162:165], v[178:181], v[132:135]
	v_mfma_f32_16x16x32_bf16 v[128:131], v[170:173], v[178:181], v[128:131]
	v_mfma_f32_16x16x32_bf16 v[100:103], v[162:165], v[186:189], v[100:103]
	v_mfma_f32_16x16x32_bf16 v[96:99], v[170:173], v[186:189], v[96:99]
	v_mfma_f32_16x16x32_bf16 v[84:87], v[162:165], v[194:197], v[84:87]
	v_mfma_f32_16x16x32_bf16 v[80:83], v[170:173], v[194:197], v[80:83]
	v_mfma_f32_16x16x32_bf16 v[68:71], v[162:165], v[202:205], v[68:71]
	v_mfma_f32_16x16x32_bf16 v[64:67], v[170:173], v[202:205], v[64:67]
	s_barrier
	s_setprio 0
	s_mov_b32 m0, s30
	v_lshl_add_u64 v[206:207], s[50:51], 0, v[146:147]
	s_add_u32 s0, s50, 0x4000
	ds_read_b128 v[174:177], v157 offset:16384
	ds_read_b128 v[178:181], v157 offset:17408
	ds_read_b128 v[182:185], v157 offset:18432
	ds_read_b128 v[186:189], v157 offset:19456
	ds_read_b128 v[190:193], v157 offset:20480
	ds_read_b128 v[194:197], v157 offset:21504
	ds_read_b128 v[198:201], v157 offset:22528
	ds_read_b128 v[202:205], v157 offset:23552
	global_load_lds_dwordx4 v[206:207], off
	v_lshl_add_u64 v[206:207], s[50:51], 0, v[150:151]
	s_mov_b32 m0, s31
	s_addc_u32 s1, s51, 0
	global_load_lds_dwordx4 v[206:207], off
	v_lshl_add_u64 v[206:207], s[0:1], 0, v[146:147]
	s_mov_b32 m0, s54
	s_nop 0
	global_load_lds_dwordx4 v[206:207], off
	v_lshl_add_u64 v[206:207], s[0:1], 0, v[150:151]
	s_mov_b32 m0, s55
	s_nop 0
	global_load_lds_dwordx4 v[206:207], off
	v_lshl_add_u64 v[206:207], s[52:53], 0, v[144:145]
	s_mov_b32 m0, s56
	s_nop 0
	global_load_lds_dwordx4 v[206:207], off
	v_lshl_add_u64 v[206:207], s[52:53], 0, v[148:149]
	s_mov_b32 m0, s57
	s_nop 0
	global_load_lds_dwordx4 v[206:207], off
	s_waitcnt vmcnt(8)
	s_waitcnt lgkmcnt(0)
	s_setprio 1
	s_barrier
	v_mfma_f32_16x16x32_bf16 v[60:63], v[108:111], v[174:177], 0
	v_mfma_f32_16x16x32_bf16 v[56:59], v[120:123], v[174:177], 0
	v_mfma_f32_16x16x32_bf16 v[44:47], v[108:111], v[182:185], 0
	v_mfma_f32_16x16x32_bf16 v[40:43], v[120:123], v[182:185], 0
	v_mfma_f32_16x16x32_bf16 v[28:31], v[108:111], v[190:193], 0
	v_mfma_f32_16x16x32_bf16 v[24:27], v[120:123], v[190:193], 0
	v_mfma_f32_16x16x32_bf16 v[12:15], v[108:111], v[198:201], 0
	v_mfma_f32_16x16x32_bf16 v[8:11], v[120:123], v[198:201], 0
	v_mfma_f32_16x16x32_bf16 v[60:63], v[112:115], v[178:181], v[60:63]
	v_mfma_f32_16x16x32_bf16 v[56:59], v[124:127], v[178:181], v[56:59]
	v_mfma_f32_16x16x32_bf16 v[44:47], v[112:115], v[186:189], v[44:47]
	v_mfma_f32_16x16x32_bf16 v[40:43], v[124:127], v[186:189], v[40:43]
	v_mfma_f32_16x16x32_bf16 v[28:31], v[112:115], v[194:197], v[28:31]
	v_mfma_f32_16x16x32_bf16 v[24:27], v[124:127], v[194:197], v[24:27]
	v_mfma_f32_16x16x32_bf16 v[12:15], v[112:115], v[202:205], v[12:15]
	v_mfma_f32_16x16x32_bf16 v[8:11], v[124:127], v[202:205], v[8:11]
	s_setprio 0
	s_setprio 1
	v_mfma_f32_16x16x32_bf16 v[52:55], v[158:161], v[174:177], 0
	v_mfma_f32_16x16x32_bf16 v[48:51], v[166:169], v[174:177], 0
	v_mfma_f32_16x16x32_bf16 v[36:39], v[158:161], v[182:185], 0
	v_mfma_f32_16x16x32_bf16 v[32:35], v[166:169], v[182:185], 0
	v_mfma_f32_16x16x32_bf16 v[20:23], v[158:161], v[190:193], 0
	v_mfma_f32_16x16x32_bf16 v[16:19], v[166:169], v[190:193], 0
	v_mfma_f32_16x16x32_bf16 v[4:7], v[158:161], v[198:201], 0
	v_mfma_f32_16x16x32_bf16 v[0:3], v[166:169], v[198:201], 0
	v_mfma_f32_16x16x32_bf16 v[52:55], v[162:165], v[178:181], v[52:55]
	v_mfma_f32_16x16x32_bf16 v[48:51], v[170:173], v[178:181], v[48:51]
	v_mfma_f32_16x16x32_bf16 v[36:39], v[162:165], v[186:189], v[36:39]
	v_mfma_f32_16x16x32_bf16 v[32:35], v[170:173], v[186:189], v[32:35]
	v_mfma_f32_16x16x32_bf16 v[20:23], v[162:165], v[194:197], v[20:23]
	v_mfma_f32_16x16x32_bf16 v[16:19], v[170:173], v[194:197], v[16:19]
	v_mfma_f32_16x16x32_bf16 v[4:7], v[162:165], v[202:205], v[4:7]
	v_mfma_f32_16x16x32_bf16 v[0:3], v[170:173], v[202:205], v[0:3]
	s_barrier
	s_setprio 0
	v_add_u32_e32 v124, s62, v156
	v_add_u32_e32 v170, s67, v156
	ds_read_b128 v[108:111], v124
	ds_read_b128 v[112:115], v124 offset:1024
	ds_read_b128 v[120:123], v124 offset:2048
	ds_read_b128 v[124:127], v124 offset:3072
	ds_read_b128 v[158:161], v170
	ds_read_b128 v[162:165], v170 offset:1024
	ds_read_b128 v[166:169], v170 offset:2048
	ds_read_b128 v[170:173], v170 offset:3072
	s_add_u32 s0, s52, 0x4000
	s_addc_u32 s1, s53, 0
	s_mov_b32 m0, s58
	v_lshl_add_u64 v[206:207], s[0:1], 0, v[144:145]
	ds_read_b128 v[174:177], v157 offset:32768
	ds_read_b128 v[178:181], v157 offset:33792
	ds_read_b128 v[182:185], v157 offset:34816
	ds_read_b128 v[186:189], v157 offset:35840
	ds_read_b128 v[190:193], v157 offset:36864
	ds_read_b128 v[194:197], v157 offset:37888
	ds_read_b128 v[198:201], v157 offset:38912
	ds_read_b128 v[202:205], v157 offset:39936
	global_load_lds_dwordx4 v[206:207], off
	v_lshl_add_u64 v[206:207], s[0:1], 0, v[148:149]
	s_mov_b32 m0, s59
	s_nop 0
	global_load_lds_dwordx4 v[206:207], off
	s_waitcnt vmcnt(8)
	s_waitcnt lgkmcnt(0)
	s_setprio 1
	s_barrier
	v_mfma_f32_16x16x32_bf16 v[140:143], v[108:111], v[174:177], v[140:143]
	v_mfma_f32_16x16x32_bf16 v[136:139], v[120:123], v[174:177], v[136:139]
	v_mfma_f32_16x16x32_bf16 v[116:119], v[108:111], v[182:185], v[116:119]
	v_mfma_f32_16x16x32_bf16 v[104:107], v[120:123], v[182:185], v[104:107]
	v_mfma_f32_16x16x32_bf16 v[92:95], v[108:111], v[190:193], v[92:95]
	v_mfma_f32_16x16x32_bf16 v[88:91], v[120:123], v[190:193], v[88:91]
	v_mfma_f32_16x16x32_bf16 v[76:79], v[108:111], v[198:201], v[76:79]
	v_mfma_f32_16x16x32_bf16 v[72:75], v[120:123], v[198:201], v[72:75]
	v_mfma_f32_16x16x32_bf16 v[140:143], v[112:115], v[178:181], v[140:143]
	v_mfma_f32_16x16x32_bf16 v[136:139], v[124:127], v[178:181], v[136:139]
	v_mfma_f32_16x16x32_bf16 v[116:119], v[112:115], v[186:189], v[116:119]
	v_mfma_f32_16x16x32_bf16 v[104:107], v[124:127], v[186:189], v[104:107]
	v_mfma_f32_16x16x32_bf16 v[92:95], v[112:115], v[194:197], v[92:95]
	v_mfma_f32_16x16x32_bf16 v[88:91], v[124:127], v[194:197], v[88:91]
	v_mfma_f32_16x16x32_bf16 v[76:79], v[112:115], v[202:205], v[76:79]
	v_mfma_f32_16x16x32_bf16 v[72:75], v[124:127], v[202:205], v[72:75]
	s_setprio 0
	s_setprio 1
	v_mfma_f32_16x16x32_bf16 v[132:135], v[158:161], v[174:177], v[132:135]
	v_mfma_f32_16x16x32_bf16 v[128:131], v[166:169], v[174:177], v[128:131]
	v_mfma_f32_16x16x32_bf16 v[100:103], v[158:161], v[182:185], v[100:103]
	v_mfma_f32_16x16x32_bf16 v[96:99], v[166:169], v[182:185], v[96:99]
	v_mfma_f32_16x16x32_bf16 v[84:87], v[158:161], v[190:193], v[84:87]
	v_mfma_f32_16x16x32_bf16 v[80:83], v[166:169], v[190:193], v[80:83]
	v_mfma_f32_16x16x32_bf16 v[68:71], v[158:161], v[198:201], v[68:71]
	v_mfma_f32_16x16x32_bf16 v[64:67], v[166:169], v[198:201], v[64:67]
	v_mfma_f32_16x16x32_bf16 v[132:135], v[162:165], v[178:181], v[132:135]
	v_mfma_f32_16x16x32_bf16 v[128:131], v[170:173], v[178:181], v[128:131]
	v_mfma_f32_16x16x32_bf16 v[100:103], v[162:165], v[186:189], v[100:103]
	v_mfma_f32_16x16x32_bf16 v[96:99], v[170:173], v[186:189], v[96:99]
	v_mfma_f32_16x16x32_bf16 v[84:87], v[162:165], v[194:197], v[84:87]
	v_mfma_f32_16x16x32_bf16 v[80:83], v[170:173], v[194:197], v[80:83]
	v_mfma_f32_16x16x32_bf16 v[68:71], v[162:165], v[202:205], v[68:71]
	v_mfma_f32_16x16x32_bf16 v[64:67], v[170:173], v[202:205], v[64:67]
	s_barrier
	s_setprio 0
	s_add_u32 s0, s50, 0x8000
	s_addc_u32 s1, s51, 0
	s_mov_b32 m0, s63
	v_lshl_add_u64 v[206:207], s[0:1], 0, v[146:147]
	ds_read_b128 v[174:177], v157 offset:49152
	ds_read_b128 v[178:181], v157 offset:50176
	ds_read_b128 v[182:185], v157 offset:51200
	ds_read_b128 v[186:189], v157 offset:52224
	ds_read_b128 v[190:193], v157 offset:53248
	ds_read_b128 v[194:197], v157 offset:54272
	ds_read_b128 v[198:201], v157 offset:55296
	ds_read_b128 v[202:205], v157 offset:56320
	global_load_lds_dwordx4 v[206:207], off
	v_lshl_add_u64 v[206:207], s[0:1], 0, v[150:151]
	s_add_u32 s0, s50, 0xc000
	s_mov_b32 m0, s64
	s_addc_u32 s1, s51, 0
	global_load_lds_dwordx4 v[206:207], off
	v_lshl_add_u64 v[206:207], s[0:1], 0, v[146:147]
	s_mov_b32 m0, s68
	s_nop 0
	global_load_lds_dwordx4 v[206:207], off
	v_lshl_add_u64 v[206:207], s[0:1], 0, v[150:151]
	s_mov_b32 m0, s69
	s_nop 0
	global_load_lds_dwordx4 v[206:207], off
	v_lshl_add_u64 v[206:207], s[48:49], 0, v[144:145]
	s_mov_b32 m0, s65
	s_nop 0
	global_load_lds_dwordx4 v[206:207], off
	v_lshl_add_u64 v[206:207], s[48:49], 0, v[148:149]
	s_mov_b32 m0, s66
	s_nop 0
	global_load_lds_dwordx4 v[206:207], off
	s_waitcnt vmcnt(8)
	s_waitcnt lgkmcnt(0)
	s_setprio 1
	s_barrier
	v_mfma_f32_16x16x32_bf16 v[60:63], v[108:111], v[174:177], v[60:63]
	v_mfma_f32_16x16x32_bf16 v[56:59], v[120:123], v[174:177], v[56:59]
	v_mfma_f32_16x16x32_bf16 v[44:47], v[108:111], v[182:185], v[44:47]
	v_mfma_f32_16x16x32_bf16 v[40:43], v[120:123], v[182:185], v[40:43]
	v_mfma_f32_16x16x32_bf16 v[28:31], v[108:111], v[190:193], v[28:31]
	v_mfma_f32_16x16x32_bf16 v[24:27], v[120:123], v[190:193], v[24:27]
	v_mfma_f32_16x16x32_bf16 v[12:15], v[108:111], v[198:201], v[12:15]
	v_mfma_f32_16x16x32_bf16 v[8:11], v[120:123], v[198:201], v[8:11]
	v_mfma_f32_16x16x32_bf16 v[60:63], v[112:115], v[178:181], v[60:63]
	v_mfma_f32_16x16x32_bf16 v[56:59], v[124:127], v[178:181], v[56:59]
	v_mfma_f32_16x16x32_bf16 v[44:47], v[112:115], v[186:189], v[44:47]
	v_mfma_f32_16x16x32_bf16 v[40:43], v[124:127], v[186:189], v[40:43]
	v_mfma_f32_16x16x32_bf16 v[28:31], v[112:115], v[194:197], v[28:31]
	v_mfma_f32_16x16x32_bf16 v[24:27], v[124:127], v[194:197], v[24:27]
	v_mfma_f32_16x16x32_bf16 v[12:15], v[112:115], v[202:205], v[12:15]
	v_mfma_f32_16x16x32_bf16 v[8:11], v[124:127], v[202:205], v[8:11]
	s_setprio 0
	s_setprio 1
	v_mfma_f32_16x16x32_bf16 v[52:55], v[158:161], v[174:177], v[52:55]
	v_mfma_f32_16x16x32_bf16 v[48:51], v[166:169], v[174:177], v[48:51]
	v_mfma_f32_16x16x32_bf16 v[36:39], v[158:161], v[182:185], v[36:39]
	v_mfma_f32_16x16x32_bf16 v[32:35], v[166:169], v[182:185], v[32:35]
	v_mfma_f32_16x16x32_bf16 v[20:23], v[158:161], v[190:193], v[20:23]
	v_mfma_f32_16x16x32_bf16 v[16:19], v[166:169], v[190:193], v[16:19]
	v_mfma_f32_16x16x32_bf16 v[4:7], v[158:161], v[198:201], v[4:7]
	v_mfma_f32_16x16x32_bf16 v[0:3], v[166:169], v[198:201], v[0:3]
	v_mfma_f32_16x16x32_bf16 v[52:55], v[162:165], v[178:181], v[52:55]
	v_mfma_f32_16x16x32_bf16 v[48:51], v[170:173], v[178:181], v[48:51]
	v_mfma_f32_16x16x32_bf16 v[36:39], v[162:165], v[186:189], v[36:39]
	v_mfma_f32_16x16x32_bf16 v[32:35], v[170:173], v[186:189], v[32:35]
	v_mfma_f32_16x16x32_bf16 v[20:23], v[162:165], v[194:197], v[20:23]
	v_mfma_f32_16x16x32_bf16 v[16:19], v[170:173], v[194:197], v[16:19]
	v_mfma_f32_16x16x32_bf16 v[4:7], v[162:165], v[202:205], v[4:7]
	v_mfma_f32_16x16x32_bf16 v[0:3], v[170:173], v[202:205], v[0:3]
	s_barrier
	s_setprio 0
	s_add_i32 s78, s78, 2
	s_add_u32 s76, s76, 0x10000
	s_addc_u32 s77, s77, 0
	s_cmp_gt_u32 s78, 29
	s_mov_b64 s[0:1], s[46:47]
.LBB0_1173:
	v_add_u32_e32 v124, s28, v156
	v_add_u32_e32 v170, s45, v156
	ds_read_b128 v[108:111], v124
	ds_read_b128 v[112:115], v124 offset:1024
	ds_read_b128 v[120:123], v124 offset:2048
	ds_read_b128 v[124:127], v124 offset:3072
	ds_read_b128 v[158:161], v170
	ds_read_b128 v[162:165], v170 offset:1024
	ds_read_b128 v[166:169], v170 offset:2048
	ds_read_b128 v[170:173], v170 offset:3072
	s_add_u32 s46, s0, 0x10000
	s_addc_u32 s47, s1, 0
	s_cmp_eq_u32 s78, 28
	s_cselect_b32 s52, s5, s46
	s_cselect_b32 s53, s4, s47
	s_cselect_b32 s50, s39, s76
	s_cselect_b32 s51, s35, s77
	s_add_u32 s48, s52, 0x8000
	s_addc_u32 s49, s53, 0
	v_lshl_add_u64 v[206:207], s[0:1], 0, v[152:153]
	s_add_i32 m0, s56, 0xc000
	ds_read_b128 v[174:177], v157
	ds_read_b128 v[178:181], v157 offset:1024
	ds_read_b128 v[182:185], v157 offset:2048
	ds_read_b128 v[186:189], v157 offset:3072
	ds_read_b128 v[190:193], v157 offset:4096
	ds_read_b128 v[194:197], v157 offset:5120
	ds_read_b128 v[198:201], v157 offset:6144
	ds_read_b128 v[202:205], v157 offset:7168
	global_load_lds_dwordx4 v[206:207], off
	v_lshl_add_u64 v[206:207], s[0:1], 0, v[154:155]
	s_add_i32 m0, s56, 0xe000
	s_nop 0
	global_load_lds_dwordx4 v[206:207], off
	s_waitcnt vmcnt(8)
	s_waitcnt lgkmcnt(0)
	s_setprio 1
	s_barrier
	v_mfma_f32_16x16x32_bf16 v[140:143], v[108:111], v[174:177], v[140:143]
	v_mfma_f32_16x16x32_bf16 v[136:139], v[120:123], v[174:177], v[136:139]
	v_mfma_f32_16x16x32_bf16 v[116:119], v[108:111], v[182:185], v[116:119]
	v_mfma_f32_16x16x32_bf16 v[104:107], v[120:123], v[182:185], v[104:107]
	v_mfma_f32_16x16x32_bf16 v[92:95], v[108:111], v[190:193], v[92:95]
	v_mfma_f32_16x16x32_bf16 v[88:91], v[120:123], v[190:193], v[88:91]
	v_mfma_f32_16x16x32_bf16 v[76:79], v[108:111], v[198:201], v[76:79]
	v_mfma_f32_16x16x32_bf16 v[72:75], v[120:123], v[198:201], v[72:75]
	v_mfma_f32_16x16x32_bf16 v[140:143], v[112:115], v[178:181], v[140:143]
	v_mfma_f32_16x16x32_bf16 v[136:139], v[124:127], v[178:181], v[136:139]
	v_mfma_f32_16x16x32_bf16 v[116:119], v[112:115], v[186:189], v[116:119]
	v_mfma_f32_16x16x32_bf16 v[104:107], v[124:127], v[186:189], v[104:107]
	v_mfma_f32_16x16x32_bf16 v[92:95], v[112:115], v[194:197], v[92:95]
	v_mfma_f32_16x16x32_bf16 v[88:91], v[124:127], v[194:197], v[88:91]
	v_mfma_f32_16x16x32_bf16 v[76:79], v[112:115], v[202:205], v[76:79]
	v_mfma_f32_16x16x32_bf16 v[72:75], v[124:127], v[202:205], v[72:75]
	s_setprio 0
	s_setprio 1
	v_mfma_f32_16x16x32_bf16 v[132:135], v[158:161], v[174:177], v[132:135]
	v_mfma_f32_16x16x32_bf16 v[128:131], v[166:169], v[174:177], v[128:131]
	v_mfma_f32_16x16x32_bf16 v[100:103], v[158:161], v[182:185], v[100:103]
	v_mfma_f32_16x16x32_bf16 v[96:99], v[166:169], v[182:185], v[96:99]
	v_mfma_f32_16x16x32_bf16 v[84:87], v[158:161], v[190:193], v[84:87]
	v_mfma_f32_16x16x32_bf16 v[80:83], v[166:169], v[190:193], v[80:83]
	v_mfma_f32_16x16x32_bf16 v[68:71], v[158:161], v[198:201], v[68:71]
	v_mfma_f32_16x16x32_bf16 v[64:67], v[166:169], v[198:201], v[64:67]
	v_mfma_f32_16x16x32_bf16 v[132:135], v[162:165], v[178:181], v[132:135]
	v_mfma_f32_16x16x32_bf16 v[128:131], v[170:173], v[178:181], v[128:131]
	v_mfma_f32_16x16x32_bf16 v[100:103], v[162:165], v[186:189], v[100:103]
	v_mfma_f32_16x16x32_bf16 v[96:99], v[170:173], v[186:189], v[96:99]
	v_mfma_f32_16x16x32_bf16 v[84:87], v[162:165], v[194:197], v[84:87]
	v_mfma_f32_16x16x32_bf16 v[80:83], v[170:173], v[194:197], v[80:83]
	v_mfma_f32_16x16x32_bf16 v[68:71], v[162:165], v[202:205], v[68:71]
	v_mfma_f32_16x16x32_bf16 v[64:67], v[170:173], v[202:205], v[64:67]
	s_barrier
	s_setprio 0
	s_mov_b32 m0, s30
	v_lshl_add_u64 v[206:207], s[50:51], 0, v[146:147]
	s_add_u32 s0, s50, 0x4000
	ds_read_b128 v[174:177], v157 offset:16384
	ds_read_b128 v[178:181], v157 offset:17408
	ds_read_b128 v[182:185], v157 offset:18432
	ds_read_b128 v[186:189], v157 offset:19456
	ds_read_b128 v[190:193], v157 offset:20480
	ds_read_b128 v[194:197], v157 offset:21504
	ds_read_b128 v[198:201], v157 offset:22528
	ds_read_b128 v[202:205], v157 offset:23552
	global_load_lds_dwordx4 v[206:207], off
	v_lshl_add_u64 v[206:207], s[50:51], 0, v[150:151]
	s_mov_b32 m0, s31
	s_addc_u32 s1, s51, 0
	global_load_lds_dwordx4 v[206:207], off
	v_lshl_add_u64 v[206:207], s[0:1], 0, v[146:147]
	s_mov_b32 m0, s54
	s_nop 0
	global_load_lds_dwordx4 v[206:207], off
	v_lshl_add_u64 v[206:207], s[0:1], 0, v[150:151]
	s_mov_b32 m0, s55
	s_nop 0
	global_load_lds_dwordx4 v[206:207], off
	v_lshl_add_u64 v[206:207], s[52:53], 0, v[144:145]
	s_mov_b32 m0, s56
	s_nop 0
	global_load_lds_dwordx4 v[206:207], off
	v_lshl_add_u64 v[206:207], s[52:53], 0, v[148:149]
	s_mov_b32 m0, s57
	s_nop 0
	global_load_lds_dwordx4 v[206:207], off
	s_waitcnt vmcnt(8)
	s_waitcnt lgkmcnt(0)
	s_setprio 1
	s_barrier
	v_mfma_f32_16x16x32_bf16 v[60:63], v[108:111], v[174:177], v[60:63]
	v_mfma_f32_16x16x32_bf16 v[56:59], v[120:123], v[174:177], v[56:59]
	v_mfma_f32_16x16x32_bf16 v[44:47], v[108:111], v[182:185], v[44:47]
	v_mfma_f32_16x16x32_bf16 v[40:43], v[120:123], v[182:185], v[40:43]
	v_mfma_f32_16x16x32_bf16 v[28:31], v[108:111], v[190:193], v[28:31]
	v_mfma_f32_16x16x32_bf16 v[24:27], v[120:123], v[190:193], v[24:27]
	v_mfma_f32_16x16x32_bf16 v[12:15], v[108:111], v[198:201], v[12:15]
	v_mfma_f32_16x16x32_bf16 v[8:11], v[120:123], v[198:201], v[8:11]
	v_mfma_f32_16x16x32_bf16 v[60:63], v[112:115], v[178:181], v[60:63]
	v_mfma_f32_16x16x32_bf16 v[56:59], v[124:127], v[178:181], v[56:59]
	v_mfma_f32_16x16x32_bf16 v[44:47], v[112:115], v[186:189], v[44:47]
	v_mfma_f32_16x16x32_bf16 v[40:43], v[124:127], v[186:189], v[40:43]
	v_mfma_f32_16x16x32_bf16 v[28:31], v[112:115], v[194:197], v[28:31]
	v_mfma_f32_16x16x32_bf16 v[24:27], v[124:127], v[194:197], v[24:27]
	v_mfma_f32_16x16x32_bf16 v[12:15], v[112:115], v[202:205], v[12:15]
	v_mfma_f32_16x16x32_bf16 v[8:11], v[124:127], v[202:205], v[8:11]
	s_setprio 0
	s_setprio 1
	v_mfma_f32_16x16x32_bf16 v[52:55], v[158:161], v[174:177], v[52:55]
	v_mfma_f32_16x16x32_bf16 v[48:51], v[166:169], v[174:177], v[48:51]
	v_mfma_f32_16x16x32_bf16 v[36:39], v[158:161], v[182:185], v[36:39]
	v_mfma_f32_16x16x32_bf16 v[32:35], v[166:169], v[182:185], v[32:35]
	v_mfma_f32_16x16x32_bf16 v[20:23], v[158:161], v[190:193], v[20:23]
	v_mfma_f32_16x16x32_bf16 v[16:19], v[166:169], v[190:193], v[16:19]
	v_mfma_f32_16x16x32_bf16 v[4:7], v[158:161], v[198:201], v[4:7]
	v_mfma_f32_16x16x32_bf16 v[0:3], v[166:169], v[198:201], v[0:3]
	v_mfma_f32_16x16x32_bf16 v[52:55], v[162:165], v[178:181], v[52:55]
	v_mfma_f32_16x16x32_bf16 v[48:51], v[170:173], v[178:181], v[48:51]
	v_mfma_f32_16x16x32_bf16 v[36:39], v[162:165], v[186:189], v[36:39]
	v_mfma_f32_16x16x32_bf16 v[32:35], v[170:173], v[186:189], v[32:35]
	v_mfma_f32_16x16x32_bf16 v[20:23], v[162:165], v[194:197], v[20:23]
	v_mfma_f32_16x16x32_bf16 v[16:19], v[170:173], v[194:197], v[16:19]
	v_mfma_f32_16x16x32_bf16 v[4:7], v[162:165], v[202:205], v[4:7]
	v_mfma_f32_16x16x32_bf16 v[0:3], v[170:173], v[202:205], v[0:3]
	s_barrier
	s_setprio 0
	v_add_u32_e32 v124, s62, v156
	v_add_u32_e32 v170, s67, v156
	ds_read_b128 v[108:111], v124
	ds_read_b128 v[112:115], v124 offset:1024
	ds_read_b128 v[120:123], v124 offset:2048
	ds_read_b128 v[124:127], v124 offset:3072
	ds_read_b128 v[158:161], v170
	ds_read_b128 v[162:165], v170 offset:1024
	ds_read_b128 v[166:169], v170 offset:2048
	ds_read_b128 v[170:173], v170 offset:3072
	s_add_u32 s0, s52, 0x4000
	s_addc_u32 s1, s53, 0
	s_mov_b32 m0, s58
	v_lshl_add_u64 v[206:207], s[0:1], 0, v[144:145]
	ds_read_b128 v[174:177], v157 offset:32768
	ds_read_b128 v[178:181], v157 offset:33792
	ds_read_b128 v[182:185], v157 offset:34816
	ds_read_b128 v[186:189], v157 offset:35840
	ds_read_b128 v[190:193], v157 offset:36864
	ds_read_b128 v[194:197], v157 offset:37888
	ds_read_b128 v[198:201], v157 offset:38912
	ds_read_b128 v[202:205], v157 offset:39936
	global_load_lds_dwordx4 v[206:207], off
	v_lshl_add_u64 v[206:207], s[0:1], 0, v[148:149]
	s_mov_b32 m0, s59
	s_nop 0
	global_load_lds_dwordx4 v[206:207], off
	s_waitcnt vmcnt(8)
	s_waitcnt lgkmcnt(0)
	s_setprio 1
	s_barrier
	v_mfma_f32_16x16x32_bf16 v[140:143], v[108:111], v[174:177], v[140:143]
	v_mfma_f32_16x16x32_bf16 v[136:139], v[120:123], v[174:177], v[136:139]
	v_mfma_f32_16x16x32_bf16 v[116:119], v[108:111], v[182:185], v[116:119]
	v_mfma_f32_16x16x32_bf16 v[104:107], v[120:123], v[182:185], v[104:107]
	v_mfma_f32_16x16x32_bf16 v[92:95], v[108:111], v[190:193], v[92:95]
	v_mfma_f32_16x16x32_bf16 v[88:91], v[120:123], v[190:193], v[88:91]
	v_mfma_f32_16x16x32_bf16 v[76:79], v[108:111], v[198:201], v[76:79]
	v_mfma_f32_16x16x32_bf16 v[72:75], v[120:123], v[198:201], v[72:75]
	v_mfma_f32_16x16x32_bf16 v[140:143], v[112:115], v[178:181], v[140:143]
	v_mfma_f32_16x16x32_bf16 v[136:139], v[124:127], v[178:181], v[136:139]
	v_mfma_f32_16x16x32_bf16 v[116:119], v[112:115], v[186:189], v[116:119]
	v_mfma_f32_16x16x32_bf16 v[104:107], v[124:127], v[186:189], v[104:107]
	v_mfma_f32_16x16x32_bf16 v[92:95], v[112:115], v[194:197], v[92:95]
	v_mfma_f32_16x16x32_bf16 v[88:91], v[124:127], v[194:197], v[88:91]
	v_mfma_f32_16x16x32_bf16 v[76:79], v[112:115], v[202:205], v[76:79]
	v_mfma_f32_16x16x32_bf16 v[72:75], v[124:127], v[202:205], v[72:75]
	s_setprio 0
	s_setprio 1
	v_mfma_f32_16x16x32_bf16 v[132:135], v[158:161], v[174:177], v[132:135]
	v_mfma_f32_16x16x32_bf16 v[128:131], v[166:169], v[174:177], v[128:131]
	v_mfma_f32_16x16x32_bf16 v[100:103], v[158:161], v[182:185], v[100:103]
	v_mfma_f32_16x16x32_bf16 v[96:99], v[166:169], v[182:185], v[96:99]
	v_mfma_f32_16x16x32_bf16 v[84:87], v[158:161], v[190:193], v[84:87]
	v_mfma_f32_16x16x32_bf16 v[80:83], v[166:169], v[190:193], v[80:83]
	v_mfma_f32_16x16x32_bf16 v[68:71], v[158:161], v[198:201], v[68:71]
	v_mfma_f32_16x16x32_bf16 v[64:67], v[166:169], v[198:201], v[64:67]
	v_mfma_f32_16x16x32_bf16 v[132:135], v[162:165], v[178:181], v[132:135]
	v_mfma_f32_16x16x32_bf16 v[128:131], v[170:173], v[178:181], v[128:131]
	v_mfma_f32_16x16x32_bf16 v[100:103], v[162:165], v[186:189], v[100:103]
	v_mfma_f32_16x16x32_bf16 v[96:99], v[170:173], v[186:189], v[96:99]
	v_mfma_f32_16x16x32_bf16 v[84:87], v[162:165], v[194:197], v[84:87]
	v_mfma_f32_16x16x32_bf16 v[80:83], v[170:173], v[194:197], v[80:83]
	v_mfma_f32_16x16x32_bf16 v[68:71], v[162:165], v[202:205], v[68:71]
	v_mfma_f32_16x16x32_bf16 v[64:67], v[170:173], v[202:205], v[64:67]
	s_barrier
	s_setprio 0
	s_add_u32 s0, s50, 0x8000
	s_addc_u32 s1, s51, 0
	s_mov_b32 m0, s63
	v_lshl_add_u64 v[206:207], s[0:1], 0, v[146:147]
	ds_read_b128 v[174:177], v157 offset:49152
	ds_read_b128 v[178:181], v157 offset:50176
	ds_read_b128 v[182:185], v157 offset:51200
	ds_read_b128 v[186:189], v157 offset:52224
	ds_read_b128 v[190:193], v157 offset:53248
	ds_read_b128 v[194:197], v157 offset:54272
	ds_read_b128 v[198:201], v157 offset:55296
	ds_read_b128 v[202:205], v157 offset:56320
	global_load_lds_dwordx4 v[206:207], off
	v_lshl_add_u64 v[206:207], s[0:1], 0, v[150:151]
	s_add_u32 s0, s50, 0xc000
	s_mov_b32 m0, s64
	s_addc_u32 s1, s51, 0
	global_load_lds_dwordx4 v[206:207], off
	v_lshl_add_u64 v[206:207], s[0:1], 0, v[146:147]
	s_mov_b32 m0, s68
	s_nop 0
	global_load_lds_dwordx4 v[206:207], off
	v_lshl_add_u64 v[206:207], s[0:1], 0, v[150:151]
	s_mov_b32 m0, s69
	s_nop 0
	global_load_lds_dwordx4 v[206:207], off
	v_lshl_add_u64 v[206:207], s[48:49], 0, v[144:145]
	s_mov_b32 m0, s65
	s_nop 0
	global_load_lds_dwordx4 v[206:207], off
	v_lshl_add_u64 v[206:207], s[48:49], 0, v[148:149]
	s_mov_b32 m0, s66
	s_nop 0
	global_load_lds_dwordx4 v[206:207], off
	s_waitcnt vmcnt(8)
	s_waitcnt lgkmcnt(0)
	s_setprio 1
	s_barrier
	v_mfma_f32_16x16x32_bf16 v[60:63], v[108:111], v[174:177], v[60:63]
	v_mfma_f32_16x16x32_bf16 v[56:59], v[120:123], v[174:177], v[56:59]
	v_mfma_f32_16x16x32_bf16 v[44:47], v[108:111], v[182:185], v[44:47]
	v_mfma_f32_16x16x32_bf16 v[40:43], v[120:123], v[182:185], v[40:43]
	v_mfma_f32_16x16x32_bf16 v[28:31], v[108:111], v[190:193], v[28:31]
	v_mfma_f32_16x16x32_bf16 v[24:27], v[120:123], v[190:193], v[24:27]
	v_mfma_f32_16x16x32_bf16 v[12:15], v[108:111], v[198:201], v[12:15]
	v_mfma_f32_16x16x32_bf16 v[8:11], v[120:123], v[198:201], v[8:11]
	v_mfma_f32_16x16x32_bf16 v[60:63], v[112:115], v[178:181], v[60:63]
	v_mfma_f32_16x16x32_bf16 v[56:59], v[124:127], v[178:181], v[56:59]
	v_mfma_f32_16x16x32_bf16 v[44:47], v[112:115], v[186:189], v[44:47]
	v_mfma_f32_16x16x32_bf16 v[40:43], v[124:127], v[186:189], v[40:43]
	v_mfma_f32_16x16x32_bf16 v[28:31], v[112:115], v[194:197], v[28:31]
	v_mfma_f32_16x16x32_bf16 v[24:27], v[124:127], v[194:197], v[24:27]
	v_mfma_f32_16x16x32_bf16 v[12:15], v[112:115], v[202:205], v[12:15]
	v_mfma_f32_16x16x32_bf16 v[8:11], v[124:127], v[202:205], v[8:11]
	s_setprio 0
	s_setprio 1
	v_mfma_f32_16x16x32_bf16 v[52:55], v[158:161], v[174:177], v[52:55]
	v_mfma_f32_16x16x32_bf16 v[48:51], v[166:169], v[174:177], v[48:51]
	v_mfma_f32_16x16x32_bf16 v[36:39], v[158:161], v[182:185], v[36:39]
	v_mfma_f32_16x16x32_bf16 v[32:35], v[166:169], v[182:185], v[32:35]
	v_mfma_f32_16x16x32_bf16 v[20:23], v[158:161], v[190:193], v[20:23]
	v_mfma_f32_16x16x32_bf16 v[16:19], v[166:169], v[190:193], v[16:19]
	v_mfma_f32_16x16x32_bf16 v[4:7], v[158:161], v[198:201], v[4:7]
	v_mfma_f32_16x16x32_bf16 v[0:3], v[166:169], v[198:201], v[0:3]
	v_mfma_f32_16x16x32_bf16 v[52:55], v[162:165], v[178:181], v[52:55]
	v_mfma_f32_16x16x32_bf16 v[48:51], v[170:173], v[178:181], v[48:51]
	v_mfma_f32_16x16x32_bf16 v[36:39], v[162:165], v[186:189], v[36:39]
	v_mfma_f32_16x16x32_bf16 v[32:35], v[170:173], v[186:189], v[32:35]
	v_mfma_f32_16x16x32_bf16 v[20:23], v[162:165], v[194:197], v[20:23]
	v_mfma_f32_16x16x32_bf16 v[16:19], v[170:173], v[194:197], v[16:19]
	v_mfma_f32_16x16x32_bf16 v[4:7], v[162:165], v[202:205], v[4:7]
	v_mfma_f32_16x16x32_bf16 v[0:3], v[170:173], v[202:205], v[0:3]
	s_barrier
	s_setprio 0
	s_add_i32 s78, s78, 2
	s_add_u32 s76, s76, 0x10000
	s_addc_u32 s77, s77, 0
	s_cmp_gt_u32 s78, 29
	s_mov_b64 s[0:1], s[46:47]
	s_cbranch_scc0 .LBB0_1173
	s_and_b64 vcc, exec, s[24:25]
	s_cbranch_vccz .LBB0_1176
	s_barrier

.LBB0_1247:
	s_ashr_i32 s35, s34, 31
	s_lshl_b64 s[4:5], s[34:35], 22
	s_add_u32 s38, s17, s4
	s_addc_u32 s39, s18, s5
	s_and_b64 s[4:5], s[36:37], exec
	s_cselect_b32 s4, s39, s1
	s_cselect_b32 s5, s38, s0
	s_ashr_i32 s25, s24, 31
	s_lshl_b64 s[40:41], s[24:25], 22
	s_add_u32 s40, s19, s40
	s_addc_u32 s41, s28, s41
	s_and_b64 s[46:47], s[36:37], exec
	s_cselect_b32 s25, s41, s45
	s_cselect_b32 s35, s40, s44
	s_add_u32 s74, s44, 0x10000
	s_addc_u32 s75, s45, 0
	s_mov_b32 s76, -2
	v_add_u32_e32 v92, s30, v206
	v_add_u32_e32 v156, s52, v206
	ds_read_b128 v[72:75], v92
	ds_read_b128 v[76:79], v92 offset:1024
	ds_read_b128 v[84:87], v92 offset:2048
	ds_read_b128 v[92:95], v92 offset:3072
	ds_read_b128 v[144:147], v156
	ds_read_b128 v[148:151], v156 offset:1024
	ds_read_b128 v[152:155], v156 offset:2048
	ds_read_b128 v[156:159], v156 offset:3072
	s_add_u32 s44, s0, 0x10000
	s_addc_u32 s45, s1, 0
	s_cmpk_eq_i32 s76, 0x7c
	s_cselect_b32 s50, s5, s44
	s_cselect_b32 s51, s4, s45
	s_cselect_b32 s48, s35, s74
	s_cselect_b32 s49, s25, s75
	s_add_u32 s46, s50, 0x8000
	s_addc_u32 s47, s51, 0
	v_lshl_add_u64 v[204:205], s[0:1], 0, v[180:181]
	s_add_i32 m0, s56, 0xc000
	ds_read_b128 v[160:163], v207
	ds_read_b128 v[164:167], v207 offset:1024
	ds_read_b128 v[168:171], v207 offset:2048
	ds_read_b128 v[184:187], v207 offset:3072
	ds_read_b128 v[188:191], v207 offset:4096
	ds_read_b128 v[192:195], v207 offset:5120
	ds_read_b128 v[196:199], v207 offset:6144
	ds_read_b128 v[200:203], v207 offset:7168
	global_load_lds_dwordx4 v[204:205], off
	v_lshl_add_u64 v[204:205], s[0:1], 0, v[182:183]
	s_add_i32 m0, s56, 0xe000
	s_nop 0
	global_load_lds_dwordx4 v[204:205], off
	s_waitcnt vmcnt(8)
	s_waitcnt lgkmcnt(0)
	s_setprio 1
	s_barrier
	v_mfma_f32_16x16x32_bf16 v[140:143], v[72:75], v[160:163], 0
	v_mfma_f32_16x16x32_bf16 v[136:139], v[84:87], v[160:163], 0
	v_mfma_f32_16x16x32_bf16 v[124:127], v[72:75], v[168:171], 0
	v_mfma_f32_16x16x32_bf16 v[120:123], v[84:87], v[168:171], 0
	v_mfma_f32_16x16x32_bf16 v[108:111], v[72:75], v[188:191], 0
	v_mfma_f32_16x16x32_bf16 v[104:107], v[84:87], v[188:191], 0
	v_mfma_f32_16x16x32_bf16 v[88:91], v[72:75], v[196:199], 0
	v_mfma_f32_16x16x32_bf16 v[80:83], v[84:87], v[196:199], 0
	v_mfma_f32_16x16x32_bf16 v[140:143], v[76:79], v[164:167], v[140:143]
	v_mfma_f32_16x16x32_bf16 v[136:139], v[92:95], v[164:167], v[136:139]
	v_mfma_f32_16x16x32_bf16 v[124:127], v[76:79], v[184:187], v[124:127]
	v_mfma_f32_16x16x32_bf16 v[120:123], v[92:95], v[184:187], v[120:123]
	v_mfma_f32_16x16x32_bf16 v[108:111], v[76:79], v[192:195], v[108:111]
	v_mfma_f32_16x16x32_bf16 v[104:107], v[92:95], v[192:195], v[104:107]
	v_mfma_f32_16x16x32_bf16 v[88:91], v[76:79], v[200:203], v[88:91]
	v_mfma_f32_16x16x32_bf16 v[80:83], v[92:95], v[200:203], v[80:83]
	s_setprio 0
	s_setprio 1
	v_mfma_f32_16x16x32_bf16 v[132:135], v[144:147], v[160:163], 0
	v_mfma_f32_16x16x32_bf16 v[128:131], v[152:155], v[160:163], 0
	v_mfma_f32_16x16x32_bf16 v[116:119], v[144:147], v[168:171], 0
	v_mfma_f32_16x16x32_bf16 v[112:115], v[152:155], v[168:171], 0
	v_mfma_f32_16x16x32_bf16 v[100:103], v[144:147], v[188:191], 0
	v_mfma_f32_16x16x32_bf16 v[96:99], v[152:155], v[188:191], 0
	v_mfma_f32_16x16x32_bf16 v[68:71], v[144:147], v[196:199], 0
	v_mfma_f32_16x16x32_bf16 v[64:67], v[152:155], v[196:199], 0
	v_mfma_f32_16x16x32_bf16 v[132:135], v[148:151], v[164:167], v[132:135]
	v_mfma_f32_16x16x32_bf16 v[128:131], v[156:159], v[164:167], v[128:131]
	v_mfma_f32_16x16x32_bf16 v[116:119], v[148:151], v[184:187], v[116:119]
	v_mfma_f32_16x16x32_bf16 v[112:115], v[156:159], v[184:187], v[112:115]
	v_mfma_f32_16x16x32_bf16 v[100:103], v[148:151], v[192:195], v[100:103]
	v_mfma_f32_16x16x32_bf16 v[96:99], v[156:159], v[192:195], v[96:99]
	v_mfma_f32_16x16x32_bf16 v[68:71], v[148:151], v[200:203], v[68:71]
	v_mfma_f32_16x16x32_bf16 v[64:67], v[156:159], v[200:203], v[64:67]
	s_barrier
	s_setprio 0
	s_mov_b32 m0, s31
	v_lshl_add_u64 v[204:205], s[48:49], 0, v[174:175]
	s_add_u32 s0, s48, 0x4000
	ds_read_b128 v[160:163], v207 offset:16384
	ds_read_b128 v[164:167], v207 offset:17408
	ds_read_b128 v[168:171], v207 offset:18432
	ds_read_b128 v[184:187], v207 offset:19456
	ds_read_b128 v[188:191], v207 offset:20480
	ds_read_b128 v[192:195], v207 offset:21504
	ds_read_b128 v[196:199], v207 offset:22528
	ds_read_b128 v[200:203], v207 offset:23552
	global_load_lds_dwordx4 v[204:205], off
	v_lshl_add_u64 v[204:205], s[48:49], 0, v[178:179]
	s_mov_b32 m0, s43
	s_addc_u32 s1, s49, 0
	global_load_lds_dwordx4 v[204:205], off
	v_lshl_add_u64 v[204:205], s[0:1], 0, v[174:175]
	s_mov_b32 m0, s53
	s_nop 0
	global_load_lds_dwordx4 v[204:205], off
	v_lshl_add_u64 v[204:205], s[0:1], 0, v[178:179]
	s_mov_b32 m0, s54
	s_nop 0
	global_load_lds_dwordx4 v[204:205], off
	v_lshl_add_u64 v[204:205], s[50:51], 0, v[172:173]
	s_mov_b32 m0, s56
	s_nop 0
	global_load_lds_dwordx4 v[204:205], off
	v_lshl_add_u64 v[204:205], s[50:51], 0, v[176:177]
	s_mov_b32 m0, s57
	s_nop 0
	global_load_lds_dwordx4 v[204:205], off
	s_waitcnt vmcnt(8)
	s_waitcnt lgkmcnt(0)
	s_setprio 1
	s_barrier
	v_mfma_f32_16x16x32_bf16 v[60:63], v[72:75], v[160:163], 0
	v_mfma_f32_16x16x32_bf16 v[56:59], v[84:87], v[160:163], 0
	v_mfma_f32_16x16x32_bf16 v[44:47], v[72:75], v[168:171], 0
	v_mfma_f32_16x16x32_bf16 v[40:43], v[84:87], v[168:171], 0
	v_mfma_f32_16x16x32_bf16 v[28:31], v[72:75], v[188:191], 0
	v_mfma_f32_16x16x32_bf16 v[24:27], v[84:87], v[188:191], 0
	v_mfma_f32_16x16x32_bf16 v[12:15], v[72:75], v[196:199], 0
	v_mfma_f32_16x16x32_bf16 v[8:11], v[84:87], v[196:199], 0
	v_mfma_f32_16x16x32_bf16 v[60:63], v[76:79], v[164:167], v[60:63]
	v_mfma_f32_16x16x32_bf16 v[56:59], v[92:95], v[164:167], v[56:59]
	v_mfma_f32_16x16x32_bf16 v[44:47], v[76:79], v[184:187], v[44:47]
	v_mfma_f32_16x16x32_bf16 v[40:43], v[92:95], v[184:187], v[40:43]
	v_mfma_f32_16x16x32_bf16 v[28:31], v[76:79], v[192:195], v[28:31]
	v_mfma_f32_16x16x32_bf16 v[24:27], v[92:95], v[192:195], v[24:27]
	v_mfma_f32_16x16x32_bf16 v[12:15], v[76:79], v[200:203], v[12:15]
	v_mfma_f32_16x16x32_bf16 v[8:11], v[92:95], v[200:203], v[8:11]
	s_setprio 0
	s_setprio 1
	v_mfma_f32_16x16x32_bf16 v[52:55], v[144:147], v[160:163], 0
	v_mfma_f32_16x16x32_bf16 v[48:51], v[152:155], v[160:163], 0
	v_mfma_f32_16x16x32_bf16 v[36:39], v[144:147], v[168:171], 0
	v_mfma_f32_16x16x32_bf16 v[32:35], v[152:155], v[168:171], 0
	v_mfma_f32_16x16x32_bf16 v[20:23], v[144:147], v[188:191], 0
	v_mfma_f32_16x16x32_bf16 v[16:19], v[152:155], v[188:191], 0
	v_mfma_f32_16x16x32_bf16 v[4:7], v[144:147], v[196:199], 0
	v_mfma_f32_16x16x32_bf16 v[0:3], v[152:155], v[196:199], 0
	v_mfma_f32_16x16x32_bf16 v[52:55], v[148:151], v[164:167], v[52:55]
	v_mfma_f32_16x16x32_bf16 v[48:51], v[156:159], v[164:167], v[48:51]
	v_mfma_f32_16x16x32_bf16 v[36:39], v[148:151], v[184:187], v[36:39]
	v_mfma_f32_16x16x32_bf16 v[32:35], v[156:159], v[184:187], v[32:35]
	v_mfma_f32_16x16x32_bf16 v[20:23], v[148:151], v[192:195], v[20:23]
	v_mfma_f32_16x16x32_bf16 v[16:19], v[156:159], v[192:195], v[16:19]
	v_mfma_f32_16x16x32_bf16 v[4:7], v[148:151], v[200:203], v[4:7]
	v_mfma_f32_16x16x32_bf16 v[0:3], v[156:159], v[200:203], v[0:3]
	s_barrier
	s_setprio 0
	v_add_u32_e32 v92, s64, v206
	v_add_u32_e32 v156, s69, v206
	ds_read_b128 v[72:75], v92
	ds_read_b128 v[76:79], v92 offset:1024
	ds_read_b128 v[84:87], v92 offset:2048
	ds_read_b128 v[92:95], v92 offset:3072
	ds_read_b128 v[144:147], v156
	ds_read_b128 v[148:151], v156 offset:1024
	ds_read_b128 v[152:155], v156 offset:2048
	ds_read_b128 v[156:159], v156 offset:3072
	s_add_u32 s0, s50, 0x4000
	s_addc_u32 s1, s51, 0
	s_mov_b32 m0, s58
	v_lshl_add_u64 v[204:205], s[0:1], 0, v[172:173]
	ds_read_b128 v[160:163], v207 offset:32768
	ds_read_b128 v[164:167], v207 offset:33792
	ds_read_b128 v[168:171], v207 offset:34816
	ds_read_b128 v[184:187], v207 offset:35840
	ds_read_b128 v[188:191], v207 offset:36864
	ds_read_b128 v[192:195], v207 offset:37888
	ds_read_b128 v[196:199], v207 offset:38912
	ds_read_b128 v[200:203], v207 offset:39936
	global_load_lds_dwordx4 v[204:205], off
	v_lshl_add_u64 v[204:205], s[0:1], 0, v[176:177]
	s_mov_b32 m0, s59
	s_nop 0
	global_load_lds_dwordx4 v[204:205], off
	s_waitcnt vmcnt(8)
	s_waitcnt lgkmcnt(0)
	s_setprio 1
	s_barrier
	v_mfma_f32_16x16x32_bf16 v[140:143], v[72:75], v[160:163], v[140:143]
	v_mfma_f32_16x16x32_bf16 v[136:139], v[84:87], v[160:163], v[136:139]
	v_mfma_f32_16x16x32_bf16 v[124:127], v[72:75], v[168:171], v[124:127]
	v_mfma_f32_16x16x32_bf16 v[120:123], v[84:87], v[168:171], v[120:123]
	v_mfma_f32_16x16x32_bf16 v[108:111], v[72:75], v[188:191], v[108:111]
	v_mfma_f32_16x16x32_bf16 v[104:107], v[84:87], v[188:191], v[104:107]
	v_mfma_f32_16x16x32_bf16 v[88:91], v[72:75], v[196:199], v[88:91]
	v_mfma_f32_16x16x32_bf16 v[80:83], v[84:87], v[196:199], v[80:83]
	v_mfma_f32_16x16x32_bf16 v[140:143], v[76:79], v[164:167], v[140:143]
	v_mfma_f32_16x16x32_bf16 v[136:139], v[92:95], v[164:167], v[136:139]
	v_mfma_f32_16x16x32_bf16 v[124:127], v[76:79], v[184:187], v[124:127]
	v_mfma_f32_16x16x32_bf16 v[120:123], v[92:95], v[184:187], v[120:123]
	v_mfma_f32_16x16x32_bf16 v[108:111], v[76:79], v[192:195], v[108:111]
	v_mfma_f32_16x16x32_bf16 v[104:107], v[92:95], v[192:195], v[104:107]
	v_mfma_f32_16x16x32_bf16 v[88:91], v[76:79], v[200:203], v[88:91]
	v_mfma_f32_16x16x32_bf16 v[80:83], v[92:95], v[200:203], v[80:83]
	s_setprio 0
	s_setprio 1
	v_mfma_f32_16x16x32_bf16 v[132:135], v[144:147], v[160:163], v[132:135]
	v_mfma_f32_16x16x32_bf16 v[128:131], v[152:155], v[160:163], v[128:131]
	v_mfma_f32_16x16x32_bf16 v[116:119], v[144:147], v[168:171], v[116:119]
	v_mfma_f32_16x16x32_bf16 v[112:115], v[152:155], v[168:171], v[112:115]
	v_mfma_f32_16x16x32_bf16 v[100:103], v[144:147], v[188:191], v[100:103]
	v_mfma_f32_16x16x32_bf16 v[96:99], v[152:155], v[188:191], v[96:99]
	v_mfma_f32_16x16x32_bf16 v[68:71], v[144:147], v[196:199], v[68:71]
	v_mfma_f32_16x16x32_bf16 v[64:67], v[152:155], v[196:199], v[64:67]
	v_mfma_f32_16x16x32_bf16 v[132:135], v[148:151], v[164:167], v[132:135]
	v_mfma_f32_16x16x32_bf16 v[128:131], v[156:159], v[164:167], v[128:131]
	v_mfma_f32_16x16x32_bf16 v[116:119], v[148:151], v[184:187], v[116:119]
	v_mfma_f32_16x16x32_bf16 v[112:115], v[156:159], v[184:187], v[112:115]
	v_mfma_f32_16x16x32_bf16 v[100:103], v[148:151], v[192:195], v[100:103]
	v_mfma_f32_16x16x32_bf16 v[96:99], v[156:159], v[192:195], v[96:99]
	v_mfma_f32_16x16x32_bf16 v[68:71], v[148:151], v[200:203], v[68:71]
	v_mfma_f32_16x16x32_bf16 v[64:67], v[156:159], v[200:203], v[64:67]
	s_barrier
	s_setprio 0
	s_add_u32 s0, s48, 0x8000
	s_addc_u32 s1, s49, 0
	s_mov_b32 m0, s65
	v_lshl_add_u64 v[204:205], s[0:1], 0, v[174:175]
	ds_read_b128 v[160:163], v207 offset:49152
	ds_read_b128 v[164:167], v207 offset:50176
	ds_read_b128 v[168:171], v207 offset:51200
	ds_read_b128 v[184:187], v207 offset:52224
	ds_read_b128 v[188:191], v207 offset:53248
	ds_read_b128 v[192:195], v207 offset:54272
	ds_read_b128 v[196:199], v207 offset:55296
	ds_read_b128 v[200:203], v207 offset:56320
	global_load_lds_dwordx4 v[204:205], off
	v_lshl_add_u64 v[204:205], s[0:1], 0, v[178:179]
	s_add_u32 s0, s48, 0xc000
	s_mov_b32 m0, s66
	s_addc_u32 s1, s49, 0
	global_load_lds_dwordx4 v[204:205], off
	v_lshl_add_u64 v[204:205], s[0:1], 0, v[174:175]
	s_mov_b32 m0, s70
	s_nop 0
	global_load_lds_dwordx4 v[204:205], off
	v_lshl_add_u64 v[204:205], s[0:1], 0, v[178:179]
	s_mov_b32 m0, s71
	s_nop 0
	global_load_lds_dwordx4 v[204:205], off
	v_lshl_add_u64 v[204:205], s[46:47], 0, v[172:173]
	s_mov_b32 m0, s67
	s_nop 0
	global_load_lds_dwordx4 v[204:205], off
	v_lshl_add_u64 v[204:205], s[46:47], 0, v[176:177]
	s_mov_b32 m0, s68
	s_nop 0
	global_load_lds_dwordx4 v[204:205], off
	s_waitcnt vmcnt(8)
	s_waitcnt lgkmcnt(0)
	s_setprio 1
	s_barrier
	v_mfma_f32_16x16x32_bf16 v[60:63], v[72:75], v[160:163], v[60:63]
	v_mfma_f32_16x16x32_bf16 v[56:59], v[84:87], v[160:163], v[56:59]
	v_mfma_f32_16x16x32_bf16 v[44:47], v[72:75], v[168:171], v[44:47]
	v_mfma_f32_16x16x32_bf16 v[40:43], v[84:87], v[168:171], v[40:43]
	v_mfma_f32_16x16x32_bf16 v[28:31], v[72:75], v[188:191], v[28:31]
	v_mfma_f32_16x16x32_bf16 v[24:27], v[84:87], v[188:191], v[24:27]
	v_mfma_f32_16x16x32_bf16 v[12:15], v[72:75], v[196:199], v[12:15]
	v_mfma_f32_16x16x32_bf16 v[8:11], v[84:87], v[196:199], v[8:11]
	v_mfma_f32_16x16x32_bf16 v[60:63], v[76:79], v[164:167], v[60:63]
	v_mfma_f32_16x16x32_bf16 v[56:59], v[92:95], v[164:167], v[56:59]
	v_mfma_f32_16x16x32_bf16 v[44:47], v[76:79], v[184:187], v[44:47]
	v_mfma_f32_16x16x32_bf16 v[40:43], v[92:95], v[184:187], v[40:43]
	v_mfma_f32_16x16x32_bf16 v[28:31], v[76:79], v[192:195], v[28:31]
	v_mfma_f32_16x16x32_bf16 v[24:27], v[92:95], v[192:195], v[24:27]
	v_mfma_f32_16x16x32_bf16 v[12:15], v[76:79], v[200:203], v[12:15]
	v_mfma_f32_16x16x32_bf16 v[8:11], v[92:95], v[200:203], v[8:11]
	s_setprio 0
	s_setprio 1
	v_mfma_f32_16x16x32_bf16 v[52:55], v[144:147], v[160:163], v[52:55]
	v_mfma_f32_16x16x32_bf16 v[48:51], v[152:155], v[160:163], v[48:51]
	v_mfma_f32_16x16x32_bf16 v[36:39], v[144:147], v[168:171], v[36:39]
	v_mfma_f32_16x16x32_bf16 v[32:35], v[152:155], v[168:171], v[32:35]
	v_mfma_f32_16x16x32_bf16 v[20:23], v[144:147], v[188:191], v[20:23]
	v_mfma_f32_16x16x32_bf16 v[16:19], v[152:155], v[188:191], v[16:19]
	v_mfma_f32_16x16x32_bf16 v[4:7], v[144:147], v[196:199], v[4:7]
	v_mfma_f32_16x16x32_bf16 v[0:3], v[152:155], v[196:199], v[0:3]
	v_mfma_f32_16x16x32_bf16 v[52:55], v[148:151], v[164:167], v[52:55]
	v_mfma_f32_16x16x32_bf16 v[48:51], v[156:159], v[164:167], v[48:51]
	v_mfma_f32_16x16x32_bf16 v[36:39], v[148:151], v[184:187], v[36:39]
	v_mfma_f32_16x16x32_bf16 v[32:35], v[156:159], v[184:187], v[32:35]
	v_mfma_f32_16x16x32_bf16 v[20:23], v[148:151], v[192:195], v[20:23]
	v_mfma_f32_16x16x32_bf16 v[16:19], v[156:159], v[192:195], v[16:19]
	v_mfma_f32_16x16x32_bf16 v[4:7], v[148:151], v[200:203], v[4:7]
	v_mfma_f32_16x16x32_bf16 v[0:3], v[156:159], v[200:203], v[0:3]
	s_barrier
	s_setprio 0
	s_add_i32 s76, s76, 2
	s_add_u32 s74, s74, 0x10000
	s_addc_u32 s75, s75, 0
	s_cmpk_gt_u32 s76, 0x7d
	s_mov_b64 s[0:1], s[44:45]
.LBB0_1248:
	v_add_u32_e32 v92, s30, v206
	v_add_u32_e32 v156, s52, v206
	ds_read_b128 v[72:75], v92
	ds_read_b128 v[76:79], v92 offset:1024
	ds_read_b128 v[84:87], v92 offset:2048
	ds_read_b128 v[92:95], v92 offset:3072
	ds_read_b128 v[144:147], v156
	ds_read_b128 v[148:151], v156 offset:1024
	ds_read_b128 v[152:155], v156 offset:2048
	ds_read_b128 v[156:159], v156 offset:3072
	s_add_u32 s44, s0, 0x10000
	s_addc_u32 s45, s1, 0
	s_cmpk_eq_i32 s76, 0x7c
	s_cselect_b32 s50, s5, s44
	s_cselect_b32 s51, s4, s45
	s_cselect_b32 s48, s35, s74
	s_cselect_b32 s49, s25, s75
	s_add_u32 s46, s50, 0x8000
	s_addc_u32 s47, s51, 0
	v_lshl_add_u64 v[204:205], s[0:1], 0, v[180:181]
	s_add_i32 m0, s56, 0xc000
	ds_read_b128 v[160:163], v207
	ds_read_b128 v[164:167], v207 offset:1024
	ds_read_b128 v[168:171], v207 offset:2048
	ds_read_b128 v[184:187], v207 offset:3072
	ds_read_b128 v[188:191], v207 offset:4096
	ds_read_b128 v[192:195], v207 offset:5120
	ds_read_b128 v[196:199], v207 offset:6144
	ds_read_b128 v[200:203], v207 offset:7168
	global_load_lds_dwordx4 v[204:205], off
	v_lshl_add_u64 v[204:205], s[0:1], 0, v[182:183]
	s_add_i32 m0, s56, 0xe000
	s_nop 0
	global_load_lds_dwordx4 v[204:205], off
	s_waitcnt vmcnt(8)
	s_waitcnt lgkmcnt(0)
	s_setprio 1
	s_barrier
	v_mfma_f32_16x16x32_bf16 v[140:143], v[72:75], v[160:163], v[140:143]
	v_mfma_f32_16x16x32_bf16 v[136:139], v[84:87], v[160:163], v[136:139]
	v_mfma_f32_16x16x32_bf16 v[124:127], v[72:75], v[168:171], v[124:127]
	v_mfma_f32_16x16x32_bf16 v[120:123], v[84:87], v[168:171], v[120:123]
	v_mfma_f32_16x16x32_bf16 v[108:111], v[72:75], v[188:191], v[108:111]
	v_mfma_f32_16x16x32_bf16 v[104:107], v[84:87], v[188:191], v[104:107]
	v_mfma_f32_16x16x32_bf16 v[88:91], v[72:75], v[196:199], v[88:91]
	v_mfma_f32_16x16x32_bf16 v[80:83], v[84:87], v[196:199], v[80:83]
	v_mfma_f32_16x16x32_bf16 v[140:143], v[76:79], v[164:167], v[140:143]
	v_mfma_f32_16x16x32_bf16 v[136:139], v[92:95], v[164:167], v[136:139]
	v_mfma_f32_16x16x32_bf16 v[124:127], v[76:79], v[184:187], v[124:127]
	v_mfma_f32_16x16x32_bf16 v[120:123], v[92:95], v[184:187], v[120:123]
	v_mfma_f32_16x16x32_bf16 v[108:111], v[76:79], v[192:195], v[108:111]
	v_mfma_f32_16x16x32_bf16 v[104:107], v[92:95], v[192:195], v[104:107]
	v_mfma_f32_16x16x32_bf16 v[88:91], v[76:79], v[200:203], v[88:91]
	v_mfma_f32_16x16x32_bf16 v[80:83], v[92:95], v[200:203], v[80:83]
	s_setprio 0
	s_setprio 1
	v_mfma_f32_16x16x32_bf16 v[132:135], v[144:147], v[160:163], v[132:135]
	v_mfma_f32_16x16x32_bf16 v[128:131], v[152:155], v[160:163], v[128:131]
	v_mfma_f32_16x16x32_bf16 v[116:119], v[144:147], v[168:171], v[116:119]
	v_mfma_f32_16x16x32_bf16 v[112:115], v[152:155], v[168:171], v[112:115]
	v_mfma_f32_16x16x32_bf16 v[100:103], v[144:147], v[188:191], v[100:103]
	v_mfma_f32_16x16x32_bf16 v[96:99], v[152:155], v[188:191], v[96:99]
	v_mfma_f32_16x16x32_bf16 v[68:71], v[144:147], v[196:199], v[68:71]
	v_mfma_f32_16x16x32_bf16 v[64:67], v[152:155], v[196:199], v[64:67]
	v_mfma_f32_16x16x32_bf16 v[132:135], v[148:151], v[164:167], v[132:135]
	v_mfma_f32_16x16x32_bf16 v[128:131], v[156:159], v[164:167], v[128:131]
	v_mfma_f32_16x16x32_bf16 v[116:119], v[148:151], v[184:187], v[116:119]
	v_mfma_f32_16x16x32_bf16 v[112:115], v[156:159], v[184:187], v[112:115]
	v_mfma_f32_16x16x32_bf16 v[100:103], v[148:151], v[192:195], v[100:103]
	v_mfma_f32_16x16x32_bf16 v[96:99], v[156:159], v[192:195], v[96:99]
	v_mfma_f32_16x16x32_bf16 v[68:71], v[148:151], v[200:203], v[68:71]
	v_mfma_f32_16x16x32_bf16 v[64:67], v[156:159], v[200:203], v[64:67]
	s_barrier
	s_setprio 0
	s_mov_b32 m0, s31
	v_lshl_add_u64 v[204:205], s[48:49], 0, v[174:175]
	s_add_u32 s0, s48, 0x4000
	ds_read_b128 v[160:163], v207 offset:16384
	ds_read_b128 v[164:167], v207 offset:17408
	ds_read_b128 v[168:171], v207 offset:18432
	ds_read_b128 v[184:187], v207 offset:19456
	ds_read_b128 v[188:191], v207 offset:20480
	ds_read_b128 v[192:195], v207 offset:21504
	ds_read_b128 v[196:199], v207 offset:22528
	ds_read_b128 v[200:203], v207 offset:23552
	global_load_lds_dwordx4 v[204:205], off
	v_lshl_add_u64 v[204:205], s[48:49], 0, v[178:179]
	s_mov_b32 m0, s43
	s_addc_u32 s1, s49, 0
	global_load_lds_dwordx4 v[204:205], off
	v_lshl_add_u64 v[204:205], s[0:1], 0, v[174:175]
	s_mov_b32 m0, s53
	s_nop 0
	global_load_lds_dwordx4 v[204:205], off
	v_lshl_add_u64 v[204:205], s[0:1], 0, v[178:179]
	s_mov_b32 m0, s54
	s_nop 0
	global_load_lds_dwordx4 v[204:205], off
	v_lshl_add_u64 v[204:205], s[50:51], 0, v[172:173]
	s_mov_b32 m0, s56
	s_nop 0
	global_load_lds_dwordx4 v[204:205], off
	v_lshl_add_u64 v[204:205], s[50:51], 0, v[176:177]
	s_mov_b32 m0, s57
	s_nop 0
	global_load_lds_dwordx4 v[204:205], off
	s_waitcnt vmcnt(8)
	s_waitcnt lgkmcnt(0)
	s_setprio 1
	s_barrier
	v_mfma_f32_16x16x32_bf16 v[60:63], v[72:75], v[160:163], v[60:63]
	v_mfma_f32_16x16x32_bf16 v[56:59], v[84:87], v[160:163], v[56:59]
	v_mfma_f32_16x16x32_bf16 v[44:47], v[72:75], v[168:171], v[44:47]
	v_mfma_f32_16x16x32_bf16 v[40:43], v[84:87], v[168:171], v[40:43]
	v_mfma_f32_16x16x32_bf16 v[28:31], v[72:75], v[188:191], v[28:31]
	v_mfma_f32_16x16x32_bf16 v[24:27], v[84:87], v[188:191], v[24:27]
	v_mfma_f32_16x16x32_bf16 v[12:15], v[72:75], v[196:199], v[12:15]
	v_mfma_f32_16x16x32_bf16 v[8:11], v[84:87], v[196:199], v[8:11]
	v_mfma_f32_16x16x32_bf16 v[60:63], v[76:79], v[164:167], v[60:63]
	v_mfma_f32_16x16x32_bf16 v[56:59], v[92:95], v[164:167], v[56:59]
	v_mfma_f32_16x16x32_bf16 v[44:47], v[76:79], v[184:187], v[44:47]
	v_mfma_f32_16x16x32_bf16 v[40:43], v[92:95], v[184:187], v[40:43]
	v_mfma_f32_16x16x32_bf16 v[28:31], v[76:79], v[192:195], v[28:31]
	v_mfma_f32_16x16x32_bf16 v[24:27], v[92:95], v[192:195], v[24:27]
	v_mfma_f32_16x16x32_bf16 v[12:15], v[76:79], v[200:203], v[12:15]
	v_mfma_f32_16x16x32_bf16 v[8:11], v[92:95], v[200:203], v[8:11]
	s_setprio 0
	s_setprio 1
	v_mfma_f32_16x16x32_bf16 v[52:55], v[144:147], v[160:163], v[52:55]
	v_mfma_f32_16x16x32_bf16 v[48:51], v[152:155], v[160:163], v[48:51]
	v_mfma_f32_16x16x32_bf16 v[36:39], v[144:147], v[168:171], v[36:39]
	v_mfma_f32_16x16x32_bf16 v[32:35], v[152:155], v[168:171], v[32:35]
	v_mfma_f32_16x16x32_bf16 v[20:23], v[144:147], v[188:191], v[20:23]
	v_mfma_f32_16x16x32_bf16 v[16:19], v[152:155], v[188:191], v[16:19]
	v_mfma_f32_16x16x32_bf16 v[4:7], v[144:147], v[196:199], v[4:7]
	v_mfma_f32_16x16x32_bf16 v[0:3], v[152:155], v[196:199], v[0:3]
	v_mfma_f32_16x16x32_bf16 v[52:55], v[148:151], v[164:167], v[52:55]
	v_mfma_f32_16x16x32_bf16 v[48:51], v[156:159], v[164:167], v[48:51]
	v_mfma_f32_16x16x32_bf16 v[36:39], v[148:151], v[184:187], v[36:39]
	v_mfma_f32_16x16x32_bf16 v[32:35], v[156:159], v[184:187], v[32:35]
	v_mfma_f32_16x16x32_bf16 v[20:23], v[148:151], v[192:195], v[20:23]
	v_mfma_f32_16x16x32_bf16 v[16:19], v[156:159], v[192:195], v[16:19]
	v_mfma_f32_16x16x32_bf16 v[4:7], v[148:151], v[200:203], v[4:7]
	v_mfma_f32_16x16x32_bf16 v[0:3], v[156:159], v[200:203], v[0:3]
	s_barrier
	s_setprio 0
	v_add_u32_e32 v92, s64, v206
	v_add_u32_e32 v156, s69, v206
	ds_read_b128 v[72:75], v92
	ds_read_b128 v[76:79], v92 offset:1024
	ds_read_b128 v[84:87], v92 offset:2048
	ds_read_b128 v[92:95], v92 offset:3072
	ds_read_b128 v[144:147], v156
	ds_read_b128 v[148:151], v156 offset:1024
	ds_read_b128 v[152:155], v156 offset:2048
	ds_read_b128 v[156:159], v156 offset:3072
	s_add_u32 s0, s50, 0x4000
	s_addc_u32 s1, s51, 0
	s_mov_b32 m0, s58
	v_lshl_add_u64 v[204:205], s[0:1], 0, v[172:173]
	ds_read_b128 v[160:163], v207 offset:32768
	ds_read_b128 v[164:167], v207 offset:33792
	ds_read_b128 v[168:171], v207 offset:34816
	ds_read_b128 v[184:187], v207 offset:35840
	ds_read_b128 v[188:191], v207 offset:36864
	ds_read_b128 v[192:195], v207 offset:37888
	ds_read_b128 v[196:199], v207 offset:38912
	ds_read_b128 v[200:203], v207 offset:39936
	global_load_lds_dwordx4 v[204:205], off
	v_lshl_add_u64 v[204:205], s[0:1], 0, v[176:177]
	s_mov_b32 m0, s59
	s_nop 0
	global_load_lds_dwordx4 v[204:205], off
	s_waitcnt vmcnt(8)
	s_waitcnt lgkmcnt(0)
	s_setprio 1
	s_barrier
	v_mfma_f32_16x16x32_bf16 v[140:143], v[72:75], v[160:163], v[140:143]
	v_mfma_f32_16x16x32_bf16 v[136:139], v[84:87], v[160:163], v[136:139]
	v_mfma_f32_16x16x32_bf16 v[124:127], v[72:75], v[168:171], v[124:127]
	v_mfma_f32_16x16x32_bf16 v[120:123], v[84:87], v[168:171], v[120:123]
	v_mfma_f32_16x16x32_bf16 v[108:111], v[72:75], v[188:191], v[108:111]
	v_mfma_f32_16x16x32_bf16 v[104:107], v[84:87], v[188:191], v[104:107]
	v_mfma_f32_16x16x32_bf16 v[88:91], v[72:75], v[196:199], v[88:91]
	v_mfma_f32_16x16x32_bf16 v[80:83], v[84:87], v[196:199], v[80:83]
	v_mfma_f32_16x16x32_bf16 v[140:143], v[76:79], v[164:167], v[140:143]
	v_mfma_f32_16x16x32_bf16 v[136:139], v[92:95], v[164:167], v[136:139]
	v_mfma_f32_16x16x32_bf16 v[124:127], v[76:79], v[184:187], v[124:127]
	v_mfma_f32_16x16x32_bf16 v[120:123], v[92:95], v[184:187], v[120:123]
	v_mfma_f32_16x16x32_bf16 v[108:111], v[76:79], v[192:195], v[108:111]
	v_mfma_f32_16x16x32_bf16 v[104:107], v[92:95], v[192:195], v[104:107]
	v_mfma_f32_16x16x32_bf16 v[88:91], v[76:79], v[200:203], v[88:91]
	v_mfma_f32_16x16x32_bf16 v[80:83], v[92:95], v[200:203], v[80:83]
	s_setprio 0
	s_setprio 1
	v_mfma_f32_16x16x32_bf16 v[132:135], v[144:147], v[160:163], v[132:135]
	v_mfma_f32_16x16x32_bf16 v[128:131], v[152:155], v[160:163], v[128:131]
	v_mfma_f32_16x16x32_bf16 v[116:119], v[144:147], v[168:171], v[116:119]
	v_mfma_f32_16x16x32_bf16 v[112:115], v[152:155], v[168:171], v[112:115]
	v_mfma_f32_16x16x32_bf16 v[100:103], v[144:147], v[188:191], v[100:103]
	v_mfma_f32_16x16x32_bf16 v[96:99], v[152:155], v[188:191], v[96:99]
	v_mfma_f32_16x16x32_bf16 v[68:71], v[144:147], v[196:199], v[68:71]
	v_mfma_f32_16x16x32_bf16 v[64:67], v[152:155], v[196:199], v[64:67]
	v_mfma_f32_16x16x32_bf16 v[132:135], v[148:151], v[164:167], v[132:135]
	v_mfma_f32_16x16x32_bf16 v[128:131], v[156:159], v[164:167], v[128:131]
	v_mfma_f32_16x16x32_bf16 v[116:119], v[148:151], v[184:187], v[116:119]
	v_mfma_f32_16x16x32_bf16 v[112:115], v[156:159], v[184:187], v[112:115]
	v_mfma_f32_16x16x32_bf16 v[100:103], v[148:151], v[192:195], v[100:103]
	v_mfma_f32_16x16x32_bf16 v[96:99], v[156:159], v[192:195], v[96:99]
	v_mfma_f32_16x16x32_bf16 v[68:71], v[148:151], v[200:203], v[68:71]
	v_mfma_f32_16x16x32_bf16 v[64:67], v[156:159], v[200:203], v[64:67]
	s_barrier
	s_setprio 0
	s_add_u32 s0, s48, 0x8000
	s_addc_u32 s1, s49, 0
	s_mov_b32 m0, s65
	v_lshl_add_u64 v[204:205], s[0:1], 0, v[174:175]
	ds_read_b128 v[160:163], v207 offset:49152
	ds_read_b128 v[164:167], v207 offset:50176
	ds_read_b128 v[168:171], v207 offset:51200
	ds_read_b128 v[184:187], v207 offset:52224
	ds_read_b128 v[188:191], v207 offset:53248
	ds_read_b128 v[192:195], v207 offset:54272
	ds_read_b128 v[196:199], v207 offset:55296
	ds_read_b128 v[200:203], v207 offset:56320
	global_load_lds_dwordx4 v[204:205], off
	v_lshl_add_u64 v[204:205], s[0:1], 0, v[178:179]
	s_add_u32 s0, s48, 0xc000
	s_mov_b32 m0, s66
	s_addc_u32 s1, s49, 0
	global_load_lds_dwordx4 v[204:205], off
	v_lshl_add_u64 v[204:205], s[0:1], 0, v[174:175]
	s_mov_b32 m0, s70
	s_nop 0
	global_load_lds_dwordx4 v[204:205], off
	v_lshl_add_u64 v[204:205], s[0:1], 0, v[178:179]
	s_mov_b32 m0, s71
	s_nop 0
	global_load_lds_dwordx4 v[204:205], off
	v_lshl_add_u64 v[204:205], s[46:47], 0, v[172:173]
	s_mov_b32 m0, s67
	s_nop 0
	global_load_lds_dwordx4 v[204:205], off
	v_lshl_add_u64 v[204:205], s[46:47], 0, v[176:177]
	s_mov_b32 m0, s68
	s_nop 0
	global_load_lds_dwordx4 v[204:205], off
	s_waitcnt vmcnt(8)
	s_waitcnt lgkmcnt(0)
	s_setprio 1
	s_barrier
	v_mfma_f32_16x16x32_bf16 v[60:63], v[72:75], v[160:163], v[60:63]
	v_mfma_f32_16x16x32_bf16 v[56:59], v[84:87], v[160:163], v[56:59]
	v_mfma_f32_16x16x32_bf16 v[44:47], v[72:75], v[168:171], v[44:47]
	v_mfma_f32_16x16x32_bf16 v[40:43], v[84:87], v[168:171], v[40:43]
	v_mfma_f32_16x16x32_bf16 v[28:31], v[72:75], v[188:191], v[28:31]
	v_mfma_f32_16x16x32_bf16 v[24:27], v[84:87], v[188:191], v[24:27]
	v_mfma_f32_16x16x32_bf16 v[12:15], v[72:75], v[196:199], v[12:15]
	v_mfma_f32_16x16x32_bf16 v[8:11], v[84:87], v[196:199], v[8:11]
	v_mfma_f32_16x16x32_bf16 v[60:63], v[76:79], v[164:167], v[60:63]
	v_mfma_f32_16x16x32_bf16 v[56:59], v[92:95], v[164:167], v[56:59]
	v_mfma_f32_16x16x32_bf16 v[44:47], v[76:79], v[184:187], v[44:47]
	v_mfma_f32_16x16x32_bf16 v[40:43], v[92:95], v[184:187], v[40:43]
	v_mfma_f32_16x16x32_bf16 v[28:31], v[76:79], v[192:195], v[28:31]
	v_mfma_f32_16x16x32_bf16 v[24:27], v[92:95], v[192:195], v[24:27]
	v_mfma_f32_16x16x32_bf16 v[12:15], v[76:79], v[200:203], v[12:15]
	v_mfma_f32_16x16x32_bf16 v[8:11], v[92:95], v[200:203], v[8:11]
	s_setprio 0
	s_setprio 1
	v_mfma_f32_16x16x32_bf16 v[52:55], v[144:147], v[160:163], v[52:55]
	v_mfma_f32_16x16x32_bf16 v[48:51], v[152:155], v[160:163], v[48:51]
	v_mfma_f32_16x16x32_bf16 v[36:39], v[144:147], v[168:171], v[36:39]
	v_mfma_f32_16x16x32_bf16 v[32:35], v[152:155], v[168:171], v[32:35]
	v_mfma_f32_16x16x32_bf16 v[20:23], v[144:147], v[188:191], v[20:23]
	v_mfma_f32_16x16x32_bf16 v[16:19], v[152:155], v[188:191], v[16:19]
	v_mfma_f32_16x16x32_bf16 v[4:7], v[144:147], v[196:199], v[4:7]
	v_mfma_f32_16x16x32_bf16 v[0:3], v[152:155], v[196:199], v[0:3]
	v_mfma_f32_16x16x32_bf16 v[52:55], v[148:151], v[164:167], v[52:55]
	v_mfma_f32_16x16x32_bf16 v[48:51], v[156:159], v[164:167], v[48:51]
	v_mfma_f32_16x16x32_bf16 v[36:39], v[148:151], v[184:187], v[36:39]
	v_mfma_f32_16x16x32_bf16 v[32:35], v[156:159], v[184:187], v[32:35]
	v_mfma_f32_16x16x32_bf16 v[20:23], v[148:151], v[192:195], v[20:23]
	v_mfma_f32_16x16x32_bf16 v[16:19], v[156:159], v[192:195], v[16:19]
	v_mfma_f32_16x16x32_bf16 v[4:7], v[148:151], v[200:203], v[4:7]
	v_mfma_f32_16x16x32_bf16 v[0:3], v[156:159], v[200:203], v[0:3]
	s_barrier
	s_setprio 0
	s_add_i32 s76, s76, 2
	s_add_u32 s74, s74, 0x10000
	s_addc_u32 s75, s75, 0
	s_cmpk_gt_u32 s76, 0x7d
	s_mov_b64 s[0:1], s[44:45]
	s_cbranch_scc0 .LBB0_1248
	s_and_b64 vcc, exec, s[22:23]
	s_cbranch_vccz .LBB0_1251
	s_barrier
